# t4 + GEMM K-loop memory sub-phases issue the LDS fragment reads first, then address arithmetic and LDS-DMA loads (22 segments)
# baseline (speedup 1.0000x reference)
.LBB0_234:
	s_add_i32 s63, 0, 0x10000
	s_add_i32 s66, 0, 0x14000
	v_add_u32_e32 v134, s63, v165
	v_add_u32_e32 v160, s66, v165
	ds_read_b128 v[114:117], v134
	ds_read_b128 v[118:121], v134 offset:1024
	ds_read_b128 v[130:133], v134 offset:2048
	ds_read_b128 v[134:137], v134 offset:3072
	ds_read_b128 v[170:173], v160
	ds_read_b128 v[174:177], v160 offset:1024
	ds_read_b128 v[200:203], v160 offset:2048
	ds_read_b128 v[204:207], v160 offset:3072
	ds_read_b128 v[208:211], v168
	ds_read_b128 v[212:215], v168 offset:1024
	ds_read_b128 v[216:219], v168 offset:2048
	ds_read_b128 v[220:223], v168 offset:3072
	ds_read_b128 v[224:227], v168 offset:4096
	ds_read_b128 v[228:231], v168 offset:5120
	ds_read_b128 v[232:235], v168 offset:6144
	ds_read_b128 v[236:239], v168 offset:7168
	s_add_u32 s38, s0, 0xfffc0080
	s_addc_u32 s39, s1, -1
	s_cmp_eq_u32 s62, 12
	s_cselect_b32 s41, s25, s39
	s_cselect_b32 s40, s58, s38
	s_cselect_b32 s39, s27, s61
	s_cselect_b32 s38, s59, s60
	v_lshl_add_u64 v[160:161], s[0:1], 0, v[158:159]
	s_add_i32 m0, s37, 0xc000
	s_nop 0
	global_load_lds_dwordx4 v[160:161], off
	v_lshl_add_u64 v[160:161], s[0:1], 0, v[156:157]
	s_add_i32 m0, s37, 0xe000
	s_nop 0
	global_load_lds_dwordx4 v[160:161], off
	s_waitcnt vmcnt(8)
	s_waitcnt lgkmcnt(0)
	s_setprio 1
	s_barrier
	v_mfma_f32_16x16x32_bf16 v[142:145], v[114:117], v[208:211], v[142:145]
	v_mfma_f32_16x16x32_bf16 v[138:141], v[130:133], v[208:211], v[138:141]
	v_mfma_f32_16x16x32_bf16 v[110:113], v[114:117], v[216:219], v[110:113]
	v_mfma_f32_16x16x32_bf16 v[106:109], v[130:133], v[216:219], v[106:109]
	v_mfma_f32_16x16x32_bf16 v[94:97], v[114:117], v[224:227], v[94:97]
	v_mfma_f32_16x16x32_bf16 v[90:93], v[130:133], v[224:227], v[90:93]
	v_mfma_f32_16x16x32_bf16 v[78:81], v[114:117], v[232:235], v[78:81]
	v_mfma_f32_16x16x32_bf16 v[74:77], v[130:133], v[232:235], v[74:77]
	v_mfma_f32_16x16x32_bf16 v[142:145], v[118:121], v[212:215], v[142:145]
	v_mfma_f32_16x16x32_bf16 v[138:141], v[134:137], v[212:215], v[138:141]
	v_mfma_f32_16x16x32_bf16 v[110:113], v[118:121], v[220:223], v[110:113]
	v_mfma_f32_16x16x32_bf16 v[106:109], v[134:137], v[220:223], v[106:109]
	v_mfma_f32_16x16x32_bf16 v[94:97], v[118:121], v[228:231], v[94:97]
	v_mfma_f32_16x16x32_bf16 v[90:93], v[134:137], v[228:231], v[90:93]
	v_mfma_f32_16x16x32_bf16 v[78:81], v[118:121], v[236:239], v[78:81]
	v_mfma_f32_16x16x32_bf16 v[74:77], v[134:137], v[236:239], v[74:77]
	s_setprio 0
	s_setprio 1
	v_mfma_f32_16x16x32_bf16 v[126:129], v[170:173], v[208:211], v[126:129]
	v_mfma_f32_16x16x32_bf16 v[122:125], v[200:203], v[208:211], v[122:125]
	v_mfma_f32_16x16x32_bf16 v[102:105], v[170:173], v[216:219], v[102:105]
	v_mfma_f32_16x16x32_bf16 v[98:101], v[200:203], v[216:219], v[98:101]
	v_mfma_f32_16x16x32_bf16 v[86:89], v[170:173], v[224:227], v[86:89]
	v_mfma_f32_16x16x32_bf16 v[82:85], v[200:203], v[224:227], v[82:85]
	v_mfma_f32_16x16x32_bf16 v[70:73], v[170:173], v[232:235], v[70:73]
	v_mfma_f32_16x16x32_bf16 v[66:69], v[200:203], v[232:235], v[66:69]
	v_mfma_f32_16x16x32_bf16 v[126:129], v[174:177], v[212:215], v[126:129]
	v_mfma_f32_16x16x32_bf16 v[122:125], v[204:207], v[212:215], v[122:125]
	v_mfma_f32_16x16x32_bf16 v[102:105], v[174:177], v[220:223], v[102:105]
	v_mfma_f32_16x16x32_bf16 v[98:101], v[204:207], v[220:223], v[98:101]
	v_mfma_f32_16x16x32_bf16 v[86:89], v[174:177], v[228:231], v[86:89]
	v_mfma_f32_16x16x32_bf16 v[82:85], v[204:207], v[228:231], v[82:85]
	v_mfma_f32_16x16x32_bf16 v[70:73], v[174:177], v[236:239], v[70:73]
	v_mfma_f32_16x16x32_bf16 v[66:69], v[204:207], v[236:239], v[66:69]
	s_setprio 0
	s_barrier
	ds_read_b128 v[208:211], v168 offset:16384
	ds_read_b128 v[212:215], v168 offset:17408
	ds_read_b128 v[216:219], v168 offset:18432
	ds_read_b128 v[220:223], v168 offset:19456
	ds_read_b128 v[224:227], v168 offset:20480
	ds_read_b128 v[228:231], v168 offset:21504
	ds_read_b128 v[232:235], v168 offset:22528
	ds_read_b128 v[236:239], v168 offset:23552
	s_add_i32 s63, s63, s42
	v_lshl_add_u64 v[160:161], s[38:39], 0, v[146:147]
	s_mov_b32 m0, s63
	s_nop 0
	global_load_lds_dwordx4 v[160:161], off
	s_add_i32 m0, s63, 0x2000
	s_add_u32 s64, s38, 0x40000
	v_lshl_add_u64 v[178:179], s[38:39], 0, v[148:149]
	s_addc_u32 s65, s39, 0
	s_add_i32 s63, s66, s42
	global_load_lds_dwordx4 v[178:179], off
	v_lshl_add_u64 v[240:241], s[64:65], 0, v[146:147]
	s_mov_b32 m0, s63
	v_lshl_add_u64 v[242:243], s[40:41], 0, v[148:149]
	global_load_lds_dwordx4 v[240:241], off
	v_lshl_add_u64 v[240:241], s[64:65], 0, v[148:149]
	s_add_i32 m0, s63, 0x2000
	s_nop 0
	global_load_lds_dwordx4 v[240:241], off
	v_lshl_add_u64 v[240:241], s[40:41], 0, v[146:147]
	s_mov_b32 m0, s37
	s_nop 0
	global_load_lds_dwordx4 v[240:241], off
	s_mov_b32 m0, s47
	s_nop 0
	global_load_lds_dwordx4 v[242:243], off
	s_waitcnt vmcnt(8)
	s_waitcnt lgkmcnt(0)
	s_setprio 1
	s_barrier
	v_mfma_f32_16x16x32_bf16 v[62:65], v[114:117], v[208:211], v[62:65]
	v_mfma_f32_16x16x32_bf16 v[58:61], v[130:133], v[208:211], v[58:61]
	v_mfma_f32_16x16x32_bf16 v[46:49], v[114:117], v[216:219], v[46:49]
	v_mfma_f32_16x16x32_bf16 v[42:45], v[130:133], v[216:219], v[42:45]
	v_mfma_f32_16x16x32_bf16 v[30:33], v[114:117], v[224:227], v[30:33]
	v_mfma_f32_16x16x32_bf16 v[26:29], v[130:133], v[224:227], v[26:29]
	v_mfma_f32_16x16x32_bf16 v[14:17], v[114:117], v[232:235], v[14:17]
	v_mfma_f32_16x16x32_bf16 v[10:13], v[130:133], v[232:235], v[10:13]
	v_mfma_f32_16x16x32_bf16 v[62:65], v[118:121], v[212:215], v[62:65]
	v_mfma_f32_16x16x32_bf16 v[58:61], v[134:137], v[212:215], v[58:61]
	v_mfma_f32_16x16x32_bf16 v[46:49], v[118:121], v[220:223], v[46:49]
	v_mfma_f32_16x16x32_bf16 v[42:45], v[134:137], v[220:223], v[42:45]
	v_mfma_f32_16x16x32_bf16 v[30:33], v[118:121], v[228:231], v[30:33]
	v_mfma_f32_16x16x32_bf16 v[26:29], v[134:137], v[228:231], v[26:29]
	v_mfma_f32_16x16x32_bf16 v[14:17], v[118:121], v[236:239], v[14:17]
	v_mfma_f32_16x16x32_bf16 v[10:13], v[134:137], v[236:239], v[10:13]
	s_setprio 0
	s_setprio 1
	v_mfma_f32_16x16x32_bf16 v[54:57], v[170:173], v[208:211], v[54:57]
	v_mfma_f32_16x16x32_bf16 v[50:53], v[200:203], v[208:211], v[50:53]
	v_mfma_f32_16x16x32_bf16 v[38:41], v[170:173], v[216:219], v[38:41]
	v_mfma_f32_16x16x32_bf16 v[34:37], v[200:203], v[216:219], v[34:37]
	v_mfma_f32_16x16x32_bf16 v[22:25], v[170:173], v[224:227], v[22:25]
	v_mfma_f32_16x16x32_bf16 v[18:21], v[200:203], v[224:227], v[18:21]
	v_mfma_f32_16x16x32_bf16 v[6:9], v[170:173], v[232:235], v[6:9]
	v_mfma_f32_16x16x32_bf16 v[2:5], v[200:203], v[232:235], v[2:5]
	v_mfma_f32_16x16x32_bf16 v[54:57], v[174:177], v[212:215], v[54:57]
	v_mfma_f32_16x16x32_bf16 v[50:53], v[204:207], v[212:215], v[50:53]
	v_mfma_f32_16x16x32_bf16 v[38:41], v[174:177], v[220:223], v[38:41]
	v_mfma_f32_16x16x32_bf16 v[34:37], v[204:207], v[220:223], v[34:37]
	v_mfma_f32_16x16x32_bf16 v[22:25], v[174:177], v[228:231], v[22:25]
	v_mfma_f32_16x16x32_bf16 v[18:21], v[204:207], v[228:231], v[18:21]
	v_mfma_f32_16x16x32_bf16 v[6:9], v[174:177], v[236:239], v[6:9]
	v_mfma_f32_16x16x32_bf16 v[2:5], v[204:207], v[236:239], v[2:5]
	s_setprio 0
	s_barrier
	s_add_i32 s63, 0, 0x18000
	s_add_i32 s64, 0, 0x1c000
	v_add_u32_e32 v134, s63, v165
	v_add_u32_e32 v162, s64, v165
	ds_read_b128 v[114:117], v134
	ds_read_b128 v[118:121], v134 offset:1024
	ds_read_b128 v[130:133], v134 offset:2048
	ds_read_b128 v[134:137], v134 offset:3072
	ds_read_b128 v[170:173], v162
	ds_read_b128 v[174:177], v162 offset:1024
	ds_read_b128 v[200:203], v162 offset:2048
	ds_read_b128 v[204:207], v162 offset:3072
	ds_read_b128 v[208:211], v168 offset:32768
	ds_read_b128 v[212:215], v168 offset:33792
	ds_read_b128 v[216:219], v168 offset:34816
	ds_read_b128 v[220:223], v168 offset:35840
	ds_read_b128 v[224:227], v168 offset:36864
	ds_read_b128 v[228:231], v168 offset:37888
	ds_read_b128 v[232:235], v168 offset:38912
	ds_read_b128 v[236:239], v168 offset:39936
	s_add_u32 s40, s40, 0x40000
	s_addc_u32 s41, s41, 0
	s_mov_b32 m0, s48
	v_lshl_add_u64 v[244:245], s[40:41], 0, v[146:147]
	global_load_lds_dwordx4 v[244:245], off
	v_lshl_add_u64 v[244:245], s[40:41], 0, v[148:149]
	s_mov_b32 m0, s49
	s_nop 0
	global_load_lds_dwordx4 v[244:245], off
	s_waitcnt vmcnt(8)
	s_waitcnt lgkmcnt(0)
	s_setprio 1
	s_barrier
	v_mfma_f32_16x16x32_bf16 v[142:145], v[114:117], v[208:211], v[142:145]
	v_mfma_f32_16x16x32_bf16 v[138:141], v[130:133], v[208:211], v[138:141]
	v_mfma_f32_16x16x32_bf16 v[110:113], v[114:117], v[216:219], v[110:113]
	v_mfma_f32_16x16x32_bf16 v[106:109], v[130:133], v[216:219], v[106:109]
	v_mfma_f32_16x16x32_bf16 v[94:97], v[114:117], v[224:227], v[94:97]
	v_mfma_f32_16x16x32_bf16 v[90:93], v[130:133], v[224:227], v[90:93]
	v_mfma_f32_16x16x32_bf16 v[78:81], v[114:117], v[232:235], v[78:81]
	v_mfma_f32_16x16x32_bf16 v[74:77], v[130:133], v[232:235], v[74:77]
	v_mfma_f32_16x16x32_bf16 v[142:145], v[118:121], v[212:215], v[142:145]
	v_mfma_f32_16x16x32_bf16 v[138:141], v[134:137], v[212:215], v[138:141]
	v_mfma_f32_16x16x32_bf16 v[110:113], v[118:121], v[220:223], v[110:113]
	v_mfma_f32_16x16x32_bf16 v[106:109], v[134:137], v[220:223], v[106:109]
	v_mfma_f32_16x16x32_bf16 v[94:97], v[118:121], v[228:231], v[94:97]
	v_mfma_f32_16x16x32_bf16 v[90:93], v[134:137], v[228:231], v[90:93]
	v_mfma_f32_16x16x32_bf16 v[78:81], v[118:121], v[236:239], v[78:81]
	v_mfma_f32_16x16x32_bf16 v[74:77], v[134:137], v[236:239], v[74:77]
	s_setprio 0
	s_setprio 1
	v_mfma_f32_16x16x32_bf16 v[126:129], v[170:173], v[208:211], v[126:129]
	v_mfma_f32_16x16x32_bf16 v[122:125], v[200:203], v[208:211], v[122:125]
	v_mfma_f32_16x16x32_bf16 v[102:105], v[170:173], v[216:219], v[102:105]
	v_mfma_f32_16x16x32_bf16 v[98:101], v[200:203], v[216:219], v[98:101]
	v_mfma_f32_16x16x32_bf16 v[86:89], v[170:173], v[224:227], v[86:89]
	v_mfma_f32_16x16x32_bf16 v[82:85], v[200:203], v[224:227], v[82:85]
	v_mfma_f32_16x16x32_bf16 v[70:73], v[170:173], v[232:235], v[70:73]
	v_mfma_f32_16x16x32_bf16 v[66:69], v[200:203], v[232:235], v[66:69]
	v_mfma_f32_16x16x32_bf16 v[126:129], v[174:177], v[212:215], v[126:129]
	v_mfma_f32_16x16x32_bf16 v[122:125], v[204:207], v[212:215], v[122:125]
	v_mfma_f32_16x16x32_bf16 v[102:105], v[174:177], v[220:223], v[102:105]
	v_mfma_f32_16x16x32_bf16 v[98:101], v[204:207], v[220:223], v[98:101]
	v_mfma_f32_16x16x32_bf16 v[86:89], v[174:177], v[228:231], v[86:89]
	v_mfma_f32_16x16x32_bf16 v[82:85], v[204:207], v[228:231], v[82:85]
	v_mfma_f32_16x16x32_bf16 v[70:73], v[174:177], v[236:239], v[70:73]
	v_mfma_f32_16x16x32_bf16 v[66:69], v[204:207], v[236:239], v[66:69]
	s_setprio 0
	s_barrier
	ds_read_b128 v[208:211], v168 offset:49152
	ds_read_b128 v[212:215], v168 offset:50176
	ds_read_b128 v[216:219], v168 offset:51200
	ds_read_b128 v[220:223], v168 offset:52224
	ds_read_b128 v[224:227], v168 offset:53248
	ds_read_b128 v[228:231], v168 offset:54272
	ds_read_b128 v[232:235], v168 offset:55296
	ds_read_b128 v[236:239], v168 offset:56320
	s_add_i32 s40, s63, s42
	v_lshl_add_u64 v[160:161], v[160:161], 0, s[90:91]
	s_mov_b32 m0, s40
	s_nop 0
	global_load_lds_dwordx4 v[160:161], off
	s_add_i32 m0, s40, 0x2000
	s_add_u32 s38, s38, 0x40080
	v_lshl_add_u64 v[160:161], v[178:179], 0, s[90:91]
	s_addc_u32 s39, s39, 0
	s_add_i32 s40, s64, s42
	global_load_lds_dwordx4 v[160:161], off
	v_lshl_add_u64 v[160:161], s[38:39], 0, v[146:147]
	s_mov_b32 m0, s40
	s_nop 0
	global_load_lds_dwordx4 v[160:161], off
	v_lshl_add_u64 v[160:161], s[38:39], 0, v[148:149]
	s_add_i32 m0, s40, 0x2000
	s_nop 0
	global_load_lds_dwordx4 v[160:161], off
	v_lshl_add_u64 v[160:161], v[240:241], 0, s[90:91]
	s_mov_b32 m0, s52
	s_nop 0
	global_load_lds_dwordx4 v[160:161], off
	v_lshl_add_u64 v[160:161], v[242:243], 0, s[90:91]
	s_mov_b32 m0, s53
	s_nop 0
	global_load_lds_dwordx4 v[160:161], off
	s_waitcnt vmcnt(8)
	s_waitcnt lgkmcnt(0)
	s_setprio 1
	s_barrier
	v_mfma_f32_16x16x32_bf16 v[62:65], v[114:117], v[208:211], v[62:65]
	v_mfma_f32_16x16x32_bf16 v[58:61], v[130:133], v[208:211], v[58:61]
	v_mfma_f32_16x16x32_bf16 v[46:49], v[114:117], v[216:219], v[46:49]
	v_mfma_f32_16x16x32_bf16 v[42:45], v[130:133], v[216:219], v[42:45]
	v_mfma_f32_16x16x32_bf16 v[30:33], v[114:117], v[224:227], v[30:33]
	v_mfma_f32_16x16x32_bf16 v[26:29], v[130:133], v[224:227], v[26:29]
	v_mfma_f32_16x16x32_bf16 v[14:17], v[114:117], v[232:235], v[14:17]
	v_mfma_f32_16x16x32_bf16 v[10:13], v[130:133], v[232:235], v[10:13]
	v_mfma_f32_16x16x32_bf16 v[62:65], v[118:121], v[212:215], v[62:65]
	v_mfma_f32_16x16x32_bf16 v[58:61], v[134:137], v[212:215], v[58:61]
	v_mfma_f32_16x16x32_bf16 v[46:49], v[118:121], v[220:223], v[46:49]
	v_mfma_f32_16x16x32_bf16 v[42:45], v[134:137], v[220:223], v[42:45]
	v_mfma_f32_16x16x32_bf16 v[30:33], v[118:121], v[228:231], v[30:33]
	v_mfma_f32_16x16x32_bf16 v[26:29], v[134:137], v[228:231], v[26:29]
	v_mfma_f32_16x16x32_bf16 v[14:17], v[118:121], v[236:239], v[14:17]
	v_mfma_f32_16x16x32_bf16 v[10:13], v[134:137], v[236:239], v[10:13]
	s_setprio 0
	s_setprio 1
	v_mfma_f32_16x16x32_bf16 v[54:57], v[170:173], v[208:211], v[54:57]
	v_mfma_f32_16x16x32_bf16 v[50:53], v[200:203], v[208:211], v[50:53]
	v_mfma_f32_16x16x32_bf16 v[38:41], v[170:173], v[216:219], v[38:41]
	v_mfma_f32_16x16x32_bf16 v[34:37], v[200:203], v[216:219], v[34:37]
	v_mfma_f32_16x16x32_bf16 v[22:25], v[170:173], v[224:227], v[22:25]
	v_mfma_f32_16x16x32_bf16 v[18:21], v[200:203], v[224:227], v[18:21]
	v_mfma_f32_16x16x32_bf16 v[6:9], v[170:173], v[232:235], v[6:9]
	v_mfma_f32_16x16x32_bf16 v[2:5], v[200:203], v[232:235], v[2:5]
	v_mfma_f32_16x16x32_bf16 v[54:57], v[174:177], v[212:215], v[54:57]
	v_mfma_f32_16x16x32_bf16 v[50:53], v[204:207], v[212:215], v[50:53]
	v_mfma_f32_16x16x32_bf16 v[38:41], v[174:177], v[220:223], v[38:41]
	v_mfma_f32_16x16x32_bf16 v[34:37], v[204:207], v[220:223], v[34:37]
	v_mfma_f32_16x16x32_bf16 v[22:25], v[174:177], v[228:231], v[22:25]
	v_mfma_f32_16x16x32_bf16 v[18:21], v[204:207], v[228:231], v[18:21]
	v_mfma_f32_16x16x32_bf16 v[6:9], v[174:177], v[236:239], v[6:9]
	v_mfma_f32_16x16x32_bf16 v[2:5], v[204:207], v[236:239], v[2:5]
	s_setprio 0
	s_barrier
	s_add_i32 s62, s62, 2
	s_add_u32 s60, s60, 0x100
	s_addc_u32 s61, s61, 0
	s_add_u32 s0, s0, 0x100
	s_addc_u32 s1, s1, 0
	s_cmp_lt_u32 s62, 14
	s_cbranch_scc1 .LBB0_234
	s_andn2_b64 vcc, exec, s[22:23]
	s_cbranch_vccnz .LBB0_237
	s_barrier

.LBB0_318:
	s_add_u32 s41, s10, s40
	s_addc_u32 s42, s11, 0
	s_add_u32 s43, s41, 0x100
	s_addc_u32 s44, s42, 0
	s_and_b64 s[24:25], s[22:23], exec
	s_cselect_b32 s25, s15, s44
	s_cselect_b32 s24, s39, s43
	s_add_u32 s40, s8, s40
	s_addc_u32 s43, s9, 0
	s_add_u32 s40, s40, 0x100
	s_addc_u32 s43, s43, 0
	s_add_i32 s44, 0, 0x10000
	s_and_b64 s[22:23], s[22:23], exec
	v_add_u32_e32 v141, s44, v139
	s_cselect_b32 s23, s17, s43
	s_cselect_b32 s22, s16, s40
	s_add_i32 s43, 0, 0x14000
	ds_read_b128 v[142:145], v141
	ds_read_b128 v[146:149], v141 offset:1024
	ds_read_b128 v[150:153], v141 offset:2048
	ds_read_b128 v[154:157], v141 offset:3072
	v_add_u32_e32 v141, s43, v139
	ds_read_b128 v[158:161], v141
	ds_read_b128 v[164:167], v141 offset:1024
	ds_read_b128 v[168:171], v141 offset:2048
	ds_read_b128 v[172:175], v141 offset:3072
	s_add_u32 s40, s41, 0x20080
	s_addc_u32 s41, s42, 0
	v_lshl_add_u64 v[228:229], s[40:41], 0, v[130:131]
	s_add_i32 m0, s7, 0xc000
	ds_read_b128 v[176:179], v140
	ds_read_b128 v[200:203], v140 offset:1024
	ds_read_b128 v[204:207], v140 offset:2048
	ds_read_b128 v[208:211], v140 offset:3072
	ds_read_b128 v[212:215], v140 offset:4096
	ds_read_b128 v[216:219], v140 offset:5120
	ds_read_b128 v[220:223], v140 offset:6144
	ds_read_b128 v[224:227], v140 offset:7168
	global_load_lds_dwordx4 v[228:229], off
	v_lshl_add_u64 v[228:229], s[40:41], 0, v[132:133]
	s_add_i32 m0, s7, 0xe000
	s_nop 0
	global_load_lds_dwordx4 v[228:229], off
	s_waitcnt vmcnt(8)
	s_waitcnt lgkmcnt(0)
	s_setprio 1
	s_barrier
	v_mfma_f32_16x16x32_bf16 v[126:129], v[142:145], v[176:179], v[126:129]
	v_mfma_f32_16x16x32_bf16 v[122:125], v[150:153], v[176:179], v[122:125]
	v_mfma_f32_16x16x32_bf16 v[118:121], v[142:145], v[204:207], v[118:121]
	v_mfma_f32_16x16x32_bf16 v[114:117], v[150:153], v[204:207], v[114:117]
	v_mfma_f32_16x16x32_bf16 v[106:109], v[142:145], v[212:215], v[106:109]
	v_mfma_f32_16x16x32_bf16 v[98:101], v[150:153], v[212:215], v[98:101]
	v_mfma_f32_16x16x32_bf16 v[90:93], v[142:145], v[220:223], v[90:93]
	v_mfma_f32_16x16x32_bf16 v[82:85], v[150:153], v[220:223], v[82:85]
	v_mfma_f32_16x16x32_bf16 v[126:129], v[146:149], v[200:203], v[126:129]
	v_mfma_f32_16x16x32_bf16 v[122:125], v[154:157], v[200:203], v[122:125]
	v_mfma_f32_16x16x32_bf16 v[118:121], v[146:149], v[208:211], v[118:121]
	v_mfma_f32_16x16x32_bf16 v[114:117], v[154:157], v[208:211], v[114:117]
	v_mfma_f32_16x16x32_bf16 v[106:109], v[146:149], v[216:219], v[106:109]
	v_mfma_f32_16x16x32_bf16 v[98:101], v[154:157], v[216:219], v[98:101]
	v_mfma_f32_16x16x32_bf16 v[90:93], v[146:149], v[224:227], v[90:93]
	v_mfma_f32_16x16x32_bf16 v[82:85], v[154:157], v[224:227], v[82:85]
	s_setprio 0
	s_setprio 1
	v_mfma_f32_16x16x32_bf16 v[110:113], v[158:161], v[176:179], v[110:113]
	v_mfma_f32_16x16x32_bf16 v[102:105], v[168:171], v[176:179], v[102:105]
	v_mfma_f32_16x16x32_bf16 v[94:97], v[158:161], v[204:207], v[94:97]
	v_mfma_f32_16x16x32_bf16 v[86:89], v[168:171], v[204:207], v[86:89]
	v_mfma_f32_16x16x32_bf16 v[78:81], v[158:161], v[212:215], v[78:81]
	v_mfma_f32_16x16x32_bf16 v[74:77], v[168:171], v[212:215], v[74:77]
	v_mfma_f32_16x16x32_bf16 v[70:73], v[158:161], v[220:223], v[70:73]
	v_mfma_f32_16x16x32_bf16 v[66:69], v[168:171], v[220:223], v[66:69]
	v_mfma_f32_16x16x32_bf16 v[110:113], v[164:167], v[200:203], v[110:113]
	v_mfma_f32_16x16x32_bf16 v[102:105], v[172:175], v[200:203], v[102:105]
	v_mfma_f32_16x16x32_bf16 v[94:97], v[164:167], v[208:211], v[94:97]
	v_mfma_f32_16x16x32_bf16 v[86:89], v[172:175], v[208:211], v[86:89]
	v_mfma_f32_16x16x32_bf16 v[78:81], v[164:167], v[216:219], v[78:81]
	v_mfma_f32_16x16x32_bf16 v[74:77], v[172:175], v[216:219], v[74:77]
	v_mfma_f32_16x16x32_bf16 v[70:73], v[164:167], v[224:227], v[70:73]
	v_mfma_f32_16x16x32_bf16 v[66:69], v[172:175], v[224:227], v[66:69]
	s_setprio 0
	s_barrier
	ds_read_b128 v[176:179], v140 offset:16384
	ds_read_b128 v[200:203], v140 offset:17408
	ds_read_b128 v[204:207], v140 offset:18432
	ds_read_b128 v[208:211], v140 offset:19456
	ds_read_b128 v[212:215], v140 offset:20480
	ds_read_b128 v[216:219], v140 offset:21504
	ds_read_b128 v[220:223], v140 offset:22528
	ds_read_b128 v[224:227], v140 offset:23552
	s_add_i32 s40, s44, s31
	v_lshl_add_u64 v[228:229], s[22:23], 0, v[162:163]
	s_mov_b32 m0, s40
	s_nop 0
	global_load_lds_dwordx4 v[228:229], off
	s_add_i32 m0, s40, 0x2000
	s_add_u32 s40, s22, 0x10000
	v_lshl_add_u64 v[230:231], s[22:23], 0, v[134:135]
	s_addc_u32 s41, s23, 0
	s_add_i32 s42, s43, s31
	global_load_lds_dwordx4 v[230:231], off
	v_lshl_add_u64 v[232:233], s[40:41], 0, v[162:163]
	s_mov_b32 m0, s42
	v_lshl_add_u64 v[234:235], s[24:25], 0, v[132:133]
	global_load_lds_dwordx4 v[232:233], off
	v_lshl_add_u64 v[232:233], s[40:41], 0, v[134:135]
	s_add_i32 m0, s42, 0x2000
	s_nop 0
	global_load_lds_dwordx4 v[232:233], off
	v_lshl_add_u64 v[232:233], s[24:25], 0, v[130:131]
	s_mov_b32 m0, s7
	s_nop 0
	global_load_lds_dwordx4 v[232:233], off
	s_mov_b32 m0, s33
	s_nop 0
	global_load_lds_dwordx4 v[234:235], off
	s_waitcnt vmcnt(8)
	s_waitcnt lgkmcnt(0)
	s_setprio 1
	s_barrier
	v_mfma_f32_16x16x32_bf16 v[62:65], v[142:145], v[176:179], v[62:65]
	v_mfma_f32_16x16x32_bf16 v[58:61], v[150:153], v[176:179], v[58:61]
	v_mfma_f32_16x16x32_bf16 v[54:57], v[142:145], v[204:207], v[54:57]
	v_mfma_f32_16x16x32_bf16 v[50:53], v[150:153], v[204:207], v[50:53]
	v_mfma_f32_16x16x32_bf16 v[42:45], v[142:145], v[212:215], v[42:45]
	v_mfma_f32_16x16x32_bf16 v[34:37], v[150:153], v[212:215], v[34:37]
	v_mfma_f32_16x16x32_bf16 v[26:29], v[142:145], v[220:223], v[26:29]
	v_mfma_f32_16x16x32_bf16 v[18:21], v[150:153], v[220:223], v[18:21]
	v_mfma_f32_16x16x32_bf16 v[62:65], v[146:149], v[200:203], v[62:65]
	v_mfma_f32_16x16x32_bf16 v[58:61], v[154:157], v[200:203], v[58:61]
	v_mfma_f32_16x16x32_bf16 v[54:57], v[146:149], v[208:211], v[54:57]
	v_mfma_f32_16x16x32_bf16 v[50:53], v[154:157], v[208:211], v[50:53]
	v_mfma_f32_16x16x32_bf16 v[42:45], v[146:149], v[216:219], v[42:45]
	v_mfma_f32_16x16x32_bf16 v[34:37], v[154:157], v[216:219], v[34:37]
	v_mfma_f32_16x16x32_bf16 v[26:29], v[146:149], v[224:227], v[26:29]
	v_mfma_f32_16x16x32_bf16 v[18:21], v[154:157], v[224:227], v[18:21]
	s_setprio 0
	s_setprio 1
	v_mfma_f32_16x16x32_bf16 v[46:49], v[158:161], v[176:179], v[46:49]
	v_mfma_f32_16x16x32_bf16 v[38:41], v[168:171], v[176:179], v[38:41]
	v_mfma_f32_16x16x32_bf16 v[30:33], v[158:161], v[204:207], v[30:33]
	v_mfma_f32_16x16x32_bf16 v[22:25], v[168:171], v[204:207], v[22:25]
	v_mfma_f32_16x16x32_bf16 v[14:17], v[158:161], v[212:215], v[14:17]
	v_mfma_f32_16x16x32_bf16 v[10:13], v[168:171], v[212:215], v[10:13]
	v_mfma_f32_16x16x32_bf16 v[6:9], v[158:161], v[220:223], v[6:9]
	v_mfma_f32_16x16x32_bf16 v[2:5], v[168:171], v[220:223], v[2:5]
	v_mfma_f32_16x16x32_bf16 v[46:49], v[164:167], v[200:203], v[46:49]
	v_mfma_f32_16x16x32_bf16 v[38:41], v[172:175], v[200:203], v[38:41]
	v_mfma_f32_16x16x32_bf16 v[30:33], v[164:167], v[208:211], v[30:33]
	v_mfma_f32_16x16x32_bf16 v[22:25], v[172:175], v[208:211], v[22:25]
	v_mfma_f32_16x16x32_bf16 v[14:17], v[164:167], v[216:219], v[14:17]
	v_mfma_f32_16x16x32_bf16 v[10:13], v[172:175], v[216:219], v[10:13]
	v_mfma_f32_16x16x32_bf16 v[6:9], v[164:167], v[224:227], v[6:9]
	v_mfma_f32_16x16x32_bf16 v[2:5], v[172:175], v[224:227], v[2:5]
	s_setprio 0
	s_barrier
	s_add_i32 s40, 0, 0x18000
	v_add_u32_e32 v141, s40, v139
	s_add_i32 s41, 0, 0x1c000
	ds_read_b128 v[142:145], v141
	ds_read_b128 v[146:149], v141 offset:1024
	ds_read_b128 v[150:153], v141 offset:2048
	ds_read_b128 v[154:157], v141 offset:3072
	v_add_u32_e32 v141, s41, v139
	ds_read_b128 v[158:161], v141
	ds_read_b128 v[164:167], v141 offset:1024
	ds_read_b128 v[168:171], v141 offset:2048
	ds_read_b128 v[172:175], v141 offset:3072
	ds_read_b128 v[176:179], v140 offset:32768
	ds_read_b128 v[200:203], v140 offset:33792
	ds_read_b128 v[204:207], v140 offset:34816
	ds_read_b128 v[208:211], v140 offset:35840
	ds_read_b128 v[212:215], v140 offset:36864
	ds_read_b128 v[216:219], v140 offset:37888
	ds_read_b128 v[220:223], v140 offset:38912
	ds_read_b128 v[224:227], v140 offset:39936
	s_add_u32 s24, s24, 0x20000
	s_addc_u32 s25, s25, 0
	s_mov_b32 m0, s34
	v_lshl_add_u64 v[236:237], s[24:25], 0, v[130:131]
	global_load_lds_dwordx4 v[236:237], off
	v_lshl_add_u64 v[236:237], s[24:25], 0, v[132:133]
	s_mov_b32 m0, s35
	s_nop 0
	global_load_lds_dwordx4 v[236:237], off
	s_waitcnt vmcnt(8)
	s_waitcnt lgkmcnt(0)
	s_setprio 1
	s_barrier
	v_mfma_f32_16x16x32_bf16 v[126:129], v[142:145], v[176:179], v[126:129]
	v_mfma_f32_16x16x32_bf16 v[122:125], v[150:153], v[176:179], v[122:125]
	v_mfma_f32_16x16x32_bf16 v[118:121], v[142:145], v[204:207], v[118:121]
	v_mfma_f32_16x16x32_bf16 v[114:117], v[150:153], v[204:207], v[114:117]
	v_mfma_f32_16x16x32_bf16 v[106:109], v[142:145], v[212:215], v[106:109]
	v_mfma_f32_16x16x32_bf16 v[98:101], v[150:153], v[212:215], v[98:101]
	v_mfma_f32_16x16x32_bf16 v[90:93], v[142:145], v[220:223], v[90:93]
	v_mfma_f32_16x16x32_bf16 v[82:85], v[150:153], v[220:223], v[82:85]
	v_mfma_f32_16x16x32_bf16 v[126:129], v[146:149], v[200:203], v[126:129]
	v_mfma_f32_16x16x32_bf16 v[122:125], v[154:157], v[200:203], v[122:125]
	v_mfma_f32_16x16x32_bf16 v[118:121], v[146:149], v[208:211], v[118:121]
	v_mfma_f32_16x16x32_bf16 v[114:117], v[154:157], v[208:211], v[114:117]
	v_mfma_f32_16x16x32_bf16 v[106:109], v[146:149], v[216:219], v[106:109]
	v_mfma_f32_16x16x32_bf16 v[98:101], v[154:157], v[216:219], v[98:101]
	v_mfma_f32_16x16x32_bf16 v[90:93], v[146:149], v[224:227], v[90:93]
	v_mfma_f32_16x16x32_bf16 v[82:85], v[154:157], v[224:227], v[82:85]
	s_setprio 0
	s_setprio 1
	v_mfma_f32_16x16x32_bf16 v[110:113], v[158:161], v[176:179], v[110:113]
	v_mfma_f32_16x16x32_bf16 v[102:105], v[168:171], v[176:179], v[102:105]
	v_mfma_f32_16x16x32_bf16 v[94:97], v[158:161], v[204:207], v[94:97]
	v_mfma_f32_16x16x32_bf16 v[86:89], v[168:171], v[204:207], v[86:89]
	v_mfma_f32_16x16x32_bf16 v[78:81], v[158:161], v[212:215], v[78:81]
	v_mfma_f32_16x16x32_bf16 v[74:77], v[168:171], v[212:215], v[74:77]
	v_mfma_f32_16x16x32_bf16 v[70:73], v[158:161], v[220:223], v[70:73]
	v_mfma_f32_16x16x32_bf16 v[66:69], v[168:171], v[220:223], v[66:69]
	v_mfma_f32_16x16x32_bf16 v[110:113], v[164:167], v[200:203], v[110:113]
	v_mfma_f32_16x16x32_bf16 v[102:105], v[172:175], v[200:203], v[102:105]
	v_mfma_f32_16x16x32_bf16 v[94:97], v[164:167], v[208:211], v[94:97]
	v_mfma_f32_16x16x32_bf16 v[86:89], v[172:175], v[208:211], v[86:89]
	v_mfma_f32_16x16x32_bf16 v[78:81], v[164:167], v[216:219], v[78:81]
	v_mfma_f32_16x16x32_bf16 v[74:77], v[172:175], v[216:219], v[74:77]
	v_mfma_f32_16x16x32_bf16 v[70:73], v[164:167], v[224:227], v[70:73]
	v_mfma_f32_16x16x32_bf16 v[66:69], v[172:175], v[224:227], v[66:69]
	s_setprio 0
	s_barrier
	ds_read_b128 v[176:179], v140 offset:49152
	ds_read_b128 v[200:203], v140 offset:50176
	ds_read_b128 v[204:207], v140 offset:51200
	ds_read_b128 v[208:211], v140 offset:52224
	ds_read_b128 v[212:215], v140 offset:53248
	ds_read_b128 v[216:219], v140 offset:54272
	ds_read_b128 v[220:223], v140 offset:55296
	ds_read_b128 v[224:227], v140 offset:56320
	s_add_i32 s24, s40, s31
	v_lshl_add_u64 v[228:229], v[228:229], 0, s[90:91]
	s_mov_b32 m0, s24
	s_nop 0
	global_load_lds_dwordx4 v[228:229], off
	s_add_i32 m0, s24, 0x2000
	s_add_u32 s22, s22, 0x10080
	v_lshl_add_u64 v[228:229], v[230:231], 0, s[90:91]
	s_addc_u32 s23, s23, 0
	s_add_i32 s24, s41, s31
	global_load_lds_dwordx4 v[228:229], off
	v_lshl_add_u64 v[228:229], s[22:23], 0, v[162:163]
	s_mov_b32 m0, s24
	s_nop 0
	global_load_lds_dwordx4 v[228:229], off
	v_lshl_add_u64 v[228:229], s[22:23], 0, v[134:135]
	s_add_i32 m0, s24, 0x2000
	s_nop 0
	global_load_lds_dwordx4 v[228:229], off
	v_lshl_add_u64 v[228:229], v[232:233], 0, s[90:91]
	s_mov_b32 m0, s36
	s_nop 0
	global_load_lds_dwordx4 v[228:229], off
	v_lshl_add_u64 v[228:229], v[234:235], 0, s[90:91]
	s_mov_b32 m0, s37
	s_nop 0
	global_load_lds_dwordx4 v[228:229], off
	s_waitcnt vmcnt(8)
	s_waitcnt lgkmcnt(0)
	s_setprio 1
	s_barrier
	v_mfma_f32_16x16x32_bf16 v[62:65], v[142:145], v[176:179], v[62:65]
	v_mfma_f32_16x16x32_bf16 v[58:61], v[150:153], v[176:179], v[58:61]
	v_mfma_f32_16x16x32_bf16 v[54:57], v[142:145], v[204:207], v[54:57]
	v_mfma_f32_16x16x32_bf16 v[50:53], v[150:153], v[204:207], v[50:53]
	v_mfma_f32_16x16x32_bf16 v[42:45], v[142:145], v[212:215], v[42:45]
	v_mfma_f32_16x16x32_bf16 v[34:37], v[150:153], v[212:215], v[34:37]
	v_mfma_f32_16x16x32_bf16 v[26:29], v[142:145], v[220:223], v[26:29]
	v_mfma_f32_16x16x32_bf16 v[18:21], v[150:153], v[220:223], v[18:21]
	v_mfma_f32_16x16x32_bf16 v[62:65], v[146:149], v[200:203], v[62:65]
	v_mfma_f32_16x16x32_bf16 v[58:61], v[154:157], v[200:203], v[58:61]
	v_mfma_f32_16x16x32_bf16 v[54:57], v[146:149], v[208:211], v[54:57]
	v_mfma_f32_16x16x32_bf16 v[50:53], v[154:157], v[208:211], v[50:53]
	v_mfma_f32_16x16x32_bf16 v[42:45], v[146:149], v[216:219], v[42:45]
	v_mfma_f32_16x16x32_bf16 v[34:37], v[154:157], v[216:219], v[34:37]
	v_mfma_f32_16x16x32_bf16 v[26:29], v[146:149], v[224:227], v[26:29]
	v_mfma_f32_16x16x32_bf16 v[18:21], v[154:157], v[224:227], v[18:21]
	s_setprio 0
	s_setprio 1
	v_mfma_f32_16x16x32_bf16 v[46:49], v[158:161], v[176:179], v[46:49]
	v_mfma_f32_16x16x32_bf16 v[38:41], v[168:171], v[176:179], v[38:41]
	v_mfma_f32_16x16x32_bf16 v[30:33], v[158:161], v[204:207], v[30:33]
	v_mfma_f32_16x16x32_bf16 v[22:25], v[168:171], v[204:207], v[22:25]
	v_mfma_f32_16x16x32_bf16 v[14:17], v[158:161], v[212:215], v[14:17]
	v_mfma_f32_16x16x32_bf16 v[10:13], v[168:171], v[212:215], v[10:13]
	v_mfma_f32_16x16x32_bf16 v[6:9], v[158:161], v[220:223], v[6:9]
	v_mfma_f32_16x16x32_bf16 v[2:5], v[168:171], v[220:223], v[2:5]
	v_mfma_f32_16x16x32_bf16 v[46:49], v[164:167], v[200:203], v[46:49]
	v_mfma_f32_16x16x32_bf16 v[38:41], v[172:175], v[200:203], v[38:41]
	v_mfma_f32_16x16x32_bf16 v[30:33], v[164:167], v[208:211], v[30:33]
	v_mfma_f32_16x16x32_bf16 v[22:25], v[172:175], v[208:211], v[22:25]
	v_mfma_f32_16x16x32_bf16 v[14:17], v[164:167], v[216:219], v[14:17]
	v_mfma_f32_16x16x32_bf16 v[10:13], v[172:175], v[216:219], v[10:13]
	v_mfma_f32_16x16x32_bf16 v[6:9], v[164:167], v[224:227], v[6:9]
	v_mfma_f32_16x16x32_bf16 v[2:5], v[172:175], v[224:227], v[2:5]
	s_setprio 0
	s_barrier
	s_movk_i32 s40, 0x100
	s_and_b64 vcc, exec, s[20:21]
	s_mov_b64 s[22:23], -1
	s_mov_b64 s[20:21], 0
	s_cbranch_vccnz .LBB0_318
	s_andn2_b64 vcc, exec, s[12:13]
	s_cbranch_vccnz .LBB0_321
	s_barrier

.LBB0_775:
	s_add_i32 s42, 0, 0x10000
	v_add_u32_e32 v139, s42, v141
	s_add_i32 s44, 0, 0x14000
	ds_read_b128 v[146:149], v139
	ds_read_b128 v[150:153], v139 offset:1024
	ds_read_b128 v[154:157], v139 offset:2048
	ds_read_b128 v[158:161], v139 offset:3072
	v_add_u32_e32 v139, s44, v141
	ds_read_b128 v[164:167], v139
	ds_read_b128 v[172:175], v139 offset:1024
	ds_read_b128 v[176:179], v139 offset:2048
	ds_read_b128 v[200:203], v139 offset:3072
	ds_read_b128 v[204:207], v144
	ds_read_b128 v[208:211], v144 offset:1024
	ds_read_b128 v[212:215], v144 offset:2048
	ds_read_b128 v[216:219], v144 offset:3072
	ds_read_b128 v[220:223], v144 offset:4096
	ds_read_b128 v[224:227], v144 offset:5120
	ds_read_b128 v[228:231], v144 offset:6144
	ds_read_b128 v[232:235], v144 offset:7168
	s_add_u32 s20, s18, 0xfffe0080
	s_addc_u32 s21, s19, -1
	s_cmp_eq_u32 s41, 4
	s_cselect_b32 s23, s11, s21
	s_cselect_b32 s22, s17, s20
	s_cselect_b32 s21, s13, s40
	s_cselect_b32 s20, s12, s33
	v_lshl_add_u64 v[168:169], s[18:19], 0, v[136:137]
	s_add_i32 m0, s30, 0xc000
	s_nop 0
	global_load_lds_dwordx4 v[168:169], off
	v_lshl_add_u64 v[168:169], s[18:19], 0, v[134:135]
	s_add_i32 m0, s30, 0xe000
	s_nop 0
	global_load_lds_dwordx4 v[168:169], off
	s_waitcnt vmcnt(8)
	s_waitcnt lgkmcnt(0)
	s_setprio 1
	s_barrier
	v_mfma_f32_16x16x32_bf16 v[126:129], v[146:149], v[204:207], v[126:129]
	v_mfma_f32_16x16x32_bf16 v[122:125], v[154:157], v[204:207], v[122:125]
	v_mfma_f32_16x16x32_bf16 v[110:113], v[146:149], v[212:215], v[110:113]
	v_mfma_f32_16x16x32_bf16 v[106:109], v[154:157], v[212:215], v[106:109]
	v_mfma_f32_16x16x32_bf16 v[94:97], v[146:149], v[220:223], v[94:97]
	v_mfma_f32_16x16x32_bf16 v[90:93], v[154:157], v[220:223], v[90:93]
	v_mfma_f32_16x16x32_bf16 v[78:81], v[146:149], v[228:231], v[78:81]
	v_mfma_f32_16x16x32_bf16 v[74:77], v[154:157], v[228:231], v[74:77]
	v_mfma_f32_16x16x32_bf16 v[126:129], v[150:153], v[208:211], v[126:129]
	v_mfma_f32_16x16x32_bf16 v[122:125], v[158:161], v[208:211], v[122:125]
	v_mfma_f32_16x16x32_bf16 v[110:113], v[150:153], v[216:219], v[110:113]
	v_mfma_f32_16x16x32_bf16 v[106:109], v[158:161], v[216:219], v[106:109]
	v_mfma_f32_16x16x32_bf16 v[94:97], v[150:153], v[224:227], v[94:97]
	v_mfma_f32_16x16x32_bf16 v[90:93], v[158:161], v[224:227], v[90:93]
	v_mfma_f32_16x16x32_bf16 v[78:81], v[150:153], v[232:235], v[78:81]
	v_mfma_f32_16x16x32_bf16 v[74:77], v[158:161], v[232:235], v[74:77]
	s_setprio 0
	s_setprio 1
	v_mfma_f32_16x16x32_bf16 v[118:121], v[164:167], v[204:207], v[118:121]
	v_mfma_f32_16x16x32_bf16 v[114:117], v[176:179], v[204:207], v[114:117]
	v_mfma_f32_16x16x32_bf16 v[102:105], v[164:167], v[212:215], v[102:105]
	v_mfma_f32_16x16x32_bf16 v[98:101], v[176:179], v[212:215], v[98:101]
	v_mfma_f32_16x16x32_bf16 v[86:89], v[164:167], v[220:223], v[86:89]
	v_mfma_f32_16x16x32_bf16 v[82:85], v[176:179], v[220:223], v[82:85]
	v_mfma_f32_16x16x32_bf16 v[70:73], v[164:167], v[228:231], v[70:73]
	v_mfma_f32_16x16x32_bf16 v[66:69], v[176:179], v[228:231], v[66:69]
	v_mfma_f32_16x16x32_bf16 v[118:121], v[172:175], v[208:211], v[118:121]
	v_mfma_f32_16x16x32_bf16 v[114:117], v[200:203], v[208:211], v[114:117]
	v_mfma_f32_16x16x32_bf16 v[102:105], v[172:175], v[216:219], v[102:105]
	v_mfma_f32_16x16x32_bf16 v[98:101], v[200:203], v[216:219], v[98:101]
	v_mfma_f32_16x16x32_bf16 v[86:89], v[172:175], v[224:227], v[86:89]
	v_mfma_f32_16x16x32_bf16 v[82:85], v[200:203], v[224:227], v[82:85]
	v_mfma_f32_16x16x32_bf16 v[70:73], v[172:175], v[232:235], v[70:73]
	v_mfma_f32_16x16x32_bf16 v[66:69], v[200:203], v[232:235], v[66:69]
	s_setprio 0
	s_barrier
	ds_read_b128 v[204:207], v144 offset:16384
	ds_read_b128 v[208:211], v144 offset:17408
	ds_read_b128 v[212:215], v144 offset:18432
	ds_read_b128 v[216:219], v144 offset:19456
	ds_read_b128 v[220:223], v144 offset:20480
	ds_read_b128 v[224:227], v144 offset:21504
	ds_read_b128 v[228:231], v144 offset:22528
	ds_read_b128 v[232:235], v144 offset:23552
	s_add_i32 s42, s42, s29
	v_lshl_add_u64 v[168:169], s[20:21], 0, v[130:131]
	s_mov_b32 m0, s42
	s_nop 0
	global_load_lds_dwordx4 v[168:169], off
	s_add_i32 m0, s42, 0x2000
	s_add_u32 s42, s20, 0x20000
	v_lshl_add_u64 v[236:237], s[20:21], 0, v[132:133]
	s_addc_u32 s43, s21, 0
	s_add_i32 s44, s44, s29
	global_load_lds_dwordx4 v[236:237], off
	v_lshl_add_u64 v[238:239], s[42:43], 0, v[130:131]
	s_mov_b32 m0, s44
	v_lshl_add_u64 v[240:241], s[22:23], 0, v[132:133]
	global_load_lds_dwordx4 v[238:239], off
	v_lshl_add_u64 v[238:239], s[42:43], 0, v[132:133]
	s_add_i32 m0, s44, 0x2000
	s_nop 0
	global_load_lds_dwordx4 v[238:239], off
	v_lshl_add_u64 v[238:239], s[22:23], 0, v[130:131]
	s_mov_b32 m0, s30
	s_nop 0
	global_load_lds_dwordx4 v[238:239], off
	s_mov_b32 m0, s31
	s_nop 0
	global_load_lds_dwordx4 v[240:241], off
	s_waitcnt vmcnt(8)
	s_waitcnt lgkmcnt(0)
	s_setprio 1
	s_barrier
	v_mfma_f32_16x16x32_bf16 v[62:65], v[146:149], v[204:207], v[62:65]
	v_mfma_f32_16x16x32_bf16 v[58:61], v[154:157], v[204:207], v[58:61]
	v_mfma_f32_16x16x32_bf16 v[46:49], v[146:149], v[212:215], v[46:49]
	v_mfma_f32_16x16x32_bf16 v[42:45], v[154:157], v[212:215], v[42:45]
	v_mfma_f32_16x16x32_bf16 v[30:33], v[146:149], v[220:223], v[30:33]
	v_mfma_f32_16x16x32_bf16 v[26:29], v[154:157], v[220:223], v[26:29]
	v_mfma_f32_16x16x32_bf16 v[14:17], v[146:149], v[228:231], v[14:17]
	v_mfma_f32_16x16x32_bf16 v[10:13], v[154:157], v[228:231], v[10:13]
	v_mfma_f32_16x16x32_bf16 v[62:65], v[150:153], v[208:211], v[62:65]
	v_mfma_f32_16x16x32_bf16 v[58:61], v[158:161], v[208:211], v[58:61]
	v_mfma_f32_16x16x32_bf16 v[46:49], v[150:153], v[216:219], v[46:49]
	v_mfma_f32_16x16x32_bf16 v[42:45], v[158:161], v[216:219], v[42:45]
	v_mfma_f32_16x16x32_bf16 v[30:33], v[150:153], v[224:227], v[30:33]
	v_mfma_f32_16x16x32_bf16 v[26:29], v[158:161], v[224:227], v[26:29]
	v_mfma_f32_16x16x32_bf16 v[14:17], v[150:153], v[232:235], v[14:17]
	v_mfma_f32_16x16x32_bf16 v[10:13], v[158:161], v[232:235], v[10:13]
	s_setprio 0
	s_setprio 1
	v_mfma_f32_16x16x32_bf16 v[54:57], v[164:167], v[204:207], v[54:57]
	v_mfma_f32_16x16x32_bf16 v[50:53], v[176:179], v[204:207], v[50:53]
	v_mfma_f32_16x16x32_bf16 v[38:41], v[164:167], v[212:215], v[38:41]
	v_mfma_f32_16x16x32_bf16 v[34:37], v[176:179], v[212:215], v[34:37]
	v_mfma_f32_16x16x32_bf16 v[22:25], v[164:167], v[220:223], v[22:25]
	v_mfma_f32_16x16x32_bf16 v[18:21], v[176:179], v[220:223], v[18:21]
	v_mfma_f32_16x16x32_bf16 v[6:9], v[164:167], v[228:231], v[6:9]
	v_mfma_f32_16x16x32_bf16 v[2:5], v[176:179], v[228:231], v[2:5]
	v_mfma_f32_16x16x32_bf16 v[54:57], v[172:175], v[208:211], v[54:57]
	v_mfma_f32_16x16x32_bf16 v[50:53], v[200:203], v[208:211], v[50:53]
	v_mfma_f32_16x16x32_bf16 v[38:41], v[172:175], v[216:219], v[38:41]
	v_mfma_f32_16x16x32_bf16 v[34:37], v[200:203], v[216:219], v[34:37]
	v_mfma_f32_16x16x32_bf16 v[22:25], v[172:175], v[224:227], v[22:25]
	v_mfma_f32_16x16x32_bf16 v[18:21], v[200:203], v[224:227], v[18:21]
	v_mfma_f32_16x16x32_bf16 v[6:9], v[172:175], v[232:235], v[6:9]
	v_mfma_f32_16x16x32_bf16 v[2:5], v[200:203], v[232:235], v[2:5]
	s_setprio 0
	s_barrier
	s_add_i32 s42, 0, 0x18000
	v_add_u32_e32 v139, s42, v141
	s_add_i32 s43, 0, 0x1c000
	ds_read_b128 v[146:149], v139
	ds_read_b128 v[150:153], v139 offset:1024
	ds_read_b128 v[154:157], v139 offset:2048
	ds_read_b128 v[158:161], v139 offset:3072
	v_add_u32_e32 v139, s43, v141
	ds_read_b128 v[164:167], v139
	ds_read_b128 v[172:175], v139 offset:1024
	ds_read_b128 v[176:179], v139 offset:2048
	ds_read_b128 v[200:203], v139 offset:3072
	ds_read_b128 v[204:207], v144 offset:32768
	ds_read_b128 v[208:211], v144 offset:33792
	ds_read_b128 v[212:215], v144 offset:34816
	ds_read_b128 v[216:219], v144 offset:35840
	ds_read_b128 v[220:223], v144 offset:36864
	ds_read_b128 v[224:227], v144 offset:37888
	ds_read_b128 v[228:231], v144 offset:38912
	ds_read_b128 v[232:235], v144 offset:39936
	s_add_u32 s22, s22, 0x20000
	s_addc_u32 s23, s23, 0
	s_mov_b32 m0, s34
	v_lshl_add_u64 v[242:243], s[22:23], 0, v[130:131]
	global_load_lds_dwordx4 v[242:243], off
	v_lshl_add_u64 v[242:243], s[22:23], 0, v[132:133]
	s_mov_b32 m0, s35
	s_nop 0
	global_load_lds_dwordx4 v[242:243], off
	s_waitcnt vmcnt(8)
	s_waitcnt lgkmcnt(0)
	s_setprio 1
	s_barrier
	v_mfma_f32_16x16x32_bf16 v[126:129], v[146:149], v[204:207], v[126:129]
	v_mfma_f32_16x16x32_bf16 v[122:125], v[154:157], v[204:207], v[122:125]
	v_mfma_f32_16x16x32_bf16 v[110:113], v[146:149], v[212:215], v[110:113]
	v_mfma_f32_16x16x32_bf16 v[106:109], v[154:157], v[212:215], v[106:109]
	v_mfma_f32_16x16x32_bf16 v[94:97], v[146:149], v[220:223], v[94:97]
	v_mfma_f32_16x16x32_bf16 v[90:93], v[154:157], v[220:223], v[90:93]
	v_mfma_f32_16x16x32_bf16 v[78:81], v[146:149], v[228:231], v[78:81]
	v_mfma_f32_16x16x32_bf16 v[74:77], v[154:157], v[228:231], v[74:77]
	v_mfma_f32_16x16x32_bf16 v[126:129], v[150:153], v[208:211], v[126:129]
	v_mfma_f32_16x16x32_bf16 v[122:125], v[158:161], v[208:211], v[122:125]
	v_mfma_f32_16x16x32_bf16 v[110:113], v[150:153], v[216:219], v[110:113]
	v_mfma_f32_16x16x32_bf16 v[106:109], v[158:161], v[216:219], v[106:109]
	v_mfma_f32_16x16x32_bf16 v[94:97], v[150:153], v[224:227], v[94:97]
	v_mfma_f32_16x16x32_bf16 v[90:93], v[158:161], v[224:227], v[90:93]
	v_mfma_f32_16x16x32_bf16 v[78:81], v[150:153], v[232:235], v[78:81]
	v_mfma_f32_16x16x32_bf16 v[74:77], v[158:161], v[232:235], v[74:77]
	s_setprio 0
	s_setprio 1
	v_mfma_f32_16x16x32_bf16 v[118:121], v[164:167], v[204:207], v[118:121]
	v_mfma_f32_16x16x32_bf16 v[114:117], v[176:179], v[204:207], v[114:117]
	v_mfma_f32_16x16x32_bf16 v[102:105], v[164:167], v[212:215], v[102:105]
	v_mfma_f32_16x16x32_bf16 v[98:101], v[176:179], v[212:215], v[98:101]
	v_mfma_f32_16x16x32_bf16 v[86:89], v[164:167], v[220:223], v[86:89]
	v_mfma_f32_16x16x32_bf16 v[82:85], v[176:179], v[220:223], v[82:85]
	v_mfma_f32_16x16x32_bf16 v[70:73], v[164:167], v[228:231], v[70:73]
	v_mfma_f32_16x16x32_bf16 v[66:69], v[176:179], v[228:231], v[66:69]
	v_mfma_f32_16x16x32_bf16 v[118:121], v[172:175], v[208:211], v[118:121]
	v_mfma_f32_16x16x32_bf16 v[114:117], v[200:203], v[208:211], v[114:117]
	v_mfma_f32_16x16x32_bf16 v[102:105], v[172:175], v[216:219], v[102:105]
	v_mfma_f32_16x16x32_bf16 v[98:101], v[200:203], v[216:219], v[98:101]
	v_mfma_f32_16x16x32_bf16 v[86:89], v[172:175], v[224:227], v[86:89]
	v_mfma_f32_16x16x32_bf16 v[82:85], v[200:203], v[224:227], v[82:85]
	v_mfma_f32_16x16x32_bf16 v[70:73], v[172:175], v[232:235], v[70:73]
	v_mfma_f32_16x16x32_bf16 v[66:69], v[200:203], v[232:235], v[66:69]
	s_setprio 0
	s_barrier
	ds_read_b128 v[204:207], v144 offset:49152
	ds_read_b128 v[208:211], v144 offset:50176
	ds_read_b128 v[212:215], v144 offset:51200
	ds_read_b128 v[216:219], v144 offset:52224
	ds_read_b128 v[220:223], v144 offset:53248
	ds_read_b128 v[224:227], v144 offset:54272
	ds_read_b128 v[228:231], v144 offset:55296
	ds_read_b128 v[232:235], v144 offset:56320
	s_add_i32 s22, s42, s29
	v_lshl_add_u64 v[168:169], v[168:169], 0, s[90:91]
	s_mov_b32 m0, s22
	s_nop 0
	global_load_lds_dwordx4 v[168:169], off
	s_add_i32 m0, s22, 0x2000
	s_add_u32 s20, s20, 0x20080
	v_lshl_add_u64 v[168:169], v[236:237], 0, s[90:91]
	s_addc_u32 s21, s21, 0
	s_add_i32 s22, s43, s29
	global_load_lds_dwordx4 v[168:169], off
	v_lshl_add_u64 v[168:169], s[20:21], 0, v[130:131]
	s_mov_b32 m0, s22
	s_nop 0
	global_load_lds_dwordx4 v[168:169], off
	v_lshl_add_u64 v[168:169], s[20:21], 0, v[132:133]
	s_add_i32 m0, s22, 0x2000
	s_nop 0
	global_load_lds_dwordx4 v[168:169], off
	v_lshl_add_u64 v[168:169], v[238:239], 0, s[90:91]
	s_mov_b32 m0, s37
	s_nop 0
	global_load_lds_dwordx4 v[168:169], off
	v_lshl_add_u64 v[168:169], v[240:241], 0, s[90:91]
	s_mov_b32 m0, s38
	s_nop 0
	global_load_lds_dwordx4 v[168:169], off
	s_waitcnt vmcnt(8)
	s_waitcnt lgkmcnt(0)
	s_setprio 1
	s_barrier
	v_mfma_f32_16x16x32_bf16 v[62:65], v[146:149], v[204:207], v[62:65]
	v_mfma_f32_16x16x32_bf16 v[58:61], v[154:157], v[204:207], v[58:61]
	v_mfma_f32_16x16x32_bf16 v[46:49], v[146:149], v[212:215], v[46:49]
	v_mfma_f32_16x16x32_bf16 v[42:45], v[154:157], v[212:215], v[42:45]
	v_mfma_f32_16x16x32_bf16 v[30:33], v[146:149], v[220:223], v[30:33]
	v_mfma_f32_16x16x32_bf16 v[26:29], v[154:157], v[220:223], v[26:29]
	v_mfma_f32_16x16x32_bf16 v[14:17], v[146:149], v[228:231], v[14:17]
	v_mfma_f32_16x16x32_bf16 v[10:13], v[154:157], v[228:231], v[10:13]
	v_mfma_f32_16x16x32_bf16 v[62:65], v[150:153], v[208:211], v[62:65]
	v_mfma_f32_16x16x32_bf16 v[58:61], v[158:161], v[208:211], v[58:61]
	v_mfma_f32_16x16x32_bf16 v[46:49], v[150:153], v[216:219], v[46:49]
	v_mfma_f32_16x16x32_bf16 v[42:45], v[158:161], v[216:219], v[42:45]
	v_mfma_f32_16x16x32_bf16 v[30:33], v[150:153], v[224:227], v[30:33]
	v_mfma_f32_16x16x32_bf16 v[26:29], v[158:161], v[224:227], v[26:29]
	v_mfma_f32_16x16x32_bf16 v[14:17], v[150:153], v[232:235], v[14:17]
	v_mfma_f32_16x16x32_bf16 v[10:13], v[158:161], v[232:235], v[10:13]
	s_setprio 0
	s_setprio 1
	v_mfma_f32_16x16x32_bf16 v[54:57], v[164:167], v[204:207], v[54:57]
	v_mfma_f32_16x16x32_bf16 v[50:53], v[176:179], v[204:207], v[50:53]
	v_mfma_f32_16x16x32_bf16 v[38:41], v[164:167], v[212:215], v[38:41]
	v_mfma_f32_16x16x32_bf16 v[34:37], v[176:179], v[212:215], v[34:37]
	v_mfma_f32_16x16x32_bf16 v[22:25], v[164:167], v[220:223], v[22:25]
	v_mfma_f32_16x16x32_bf16 v[18:21], v[176:179], v[220:223], v[18:21]
	v_mfma_f32_16x16x32_bf16 v[6:9], v[164:167], v[228:231], v[6:9]
	v_mfma_f32_16x16x32_bf16 v[2:5], v[176:179], v[228:231], v[2:5]
	v_mfma_f32_16x16x32_bf16 v[54:57], v[172:175], v[208:211], v[54:57]
	v_mfma_f32_16x16x32_bf16 v[50:53], v[200:203], v[208:211], v[50:53]
	v_mfma_f32_16x16x32_bf16 v[38:41], v[172:175], v[216:219], v[38:41]
	v_mfma_f32_16x16x32_bf16 v[34:37], v[200:203], v[216:219], v[34:37]
	v_mfma_f32_16x16x32_bf16 v[22:25], v[172:175], v[224:227], v[22:25]
	v_mfma_f32_16x16x32_bf16 v[18:21], v[200:203], v[224:227], v[18:21]
	v_mfma_f32_16x16x32_bf16 v[6:9], v[172:175], v[232:235], v[6:9]
	v_mfma_f32_16x16x32_bf16 v[2:5], v[200:203], v[232:235], v[2:5]
	s_setprio 0
	s_barrier
	s_add_i32 s41, s41, 2
	s_add_u32 s33, s33, 0x100
	s_addc_u32 s40, s40, 0
	s_add_u32 s18, s18, 0x100
	s_addc_u32 s19, s19, 0
	s_cmp_lt_u32 s41, 6
	s_cbranch_scc1 .LBB0_775
	s_andn2_b64 vcc, exec, s[8:9]
	s_cbranch_vccnz .LBB0_778
	s_barrier

.LBB0_843:
	s_add_i32 s33, s26, 0x100
	s_add_u32 s41, s20, s26
	s_addc_u32 s43, s21, 0
	s_add_u32 s42, s41, 0x100
	s_addc_u32 s44, s43, 0
	s_and_b64 s[26:27], s[24:25], exec
	s_cselect_b32 s27, s13, s44
	s_cselect_b32 s26, s19, s42
	s_add_i32 s44, 0, 0x10000
	s_and_b64 s[24:25], s[24:25], exec
	s_cselect_b32 s24, 0, s33
	s_cselect_b32 s25, 0, 0
	s_add_u32 s24, s0, s24
	s_addc_u32 s25, s1, s25
	s_add_i32 s33, 0, 0x14000
	v_add_u32_e32 v134, s44, v172
	v_add_u32_e32 v158, s33, v172
	ds_read_b128 v[102:105], v134
	ds_read_b128 v[114:117], v134 offset:1024
	ds_read_b128 v[126:129], v134 offset:2048
	ds_read_b128 v[134:137], v134 offset:3072
	ds_read_b128 v[138:141], v158
	ds_read_b128 v[146:149], v158 offset:1024
	ds_read_b128 v[154:157], v158 offset:2048
	ds_read_b128 v[158:161], v158 offset:3072
	s_add_u32 s42, s41, 0x10080
	s_addc_u32 s43, s43, 0
	v_lshl_add_u64 v[224:225], s[42:43], 0, v[162:163]
	s_add_i32 m0, s34, 0xc000
	ds_read_b128 v[166:169], v173
	ds_read_b128 v[176:179], v173 offset:1024
	ds_read_b128 v[200:203], v173 offset:2048
	ds_read_b128 v[204:207], v173 offset:3072
	ds_read_b128 v[208:211], v173 offset:4096
	ds_read_b128 v[212:215], v173 offset:5120
	ds_read_b128 v[216:219], v173 offset:6144
	ds_read_b128 v[220:223], v173 offset:7168
	global_load_lds_dwordx4 v[224:225], off
	v_lshl_add_u64 v[224:225], s[42:43], 0, v[164:165]
	s_add_i32 m0, s34, 0xe000
	s_nop 0
	global_load_lds_dwordx4 v[224:225], off
	s_waitcnt vmcnt(8)
	s_waitcnt lgkmcnt(0)
	s_setprio 1
	s_barrier
	v_mfma_f32_16x16x32_bf16 v[150:153], v[102:105], v[166:169], v[150:153]
	v_mfma_f32_16x16x32_bf16 v[142:145], v[126:129], v[166:169], v[142:145]
	v_mfma_f32_16x16x32_bf16 v[118:121], v[102:105], v[200:203], v[118:121]
	v_mfma_f32_16x16x32_bf16 v[110:113], v[126:129], v[200:203], v[110:113]
	v_mfma_f32_16x16x32_bf16 v[94:97], v[102:105], v[208:211], v[94:97]
	v_mfma_f32_16x16x32_bf16 v[90:93], v[126:129], v[208:211], v[90:93]
	v_mfma_f32_16x16x32_bf16 v[78:81], v[102:105], v[216:219], v[78:81]
	v_mfma_f32_16x16x32_bf16 v[74:77], v[126:129], v[216:219], v[74:77]
	v_mfma_f32_16x16x32_bf16 v[150:153], v[114:117], v[176:179], v[150:153]
	v_mfma_f32_16x16x32_bf16 v[142:145], v[134:137], v[176:179], v[142:145]
	v_mfma_f32_16x16x32_bf16 v[118:121], v[114:117], v[204:207], v[118:121]
	v_mfma_f32_16x16x32_bf16 v[110:113], v[134:137], v[204:207], v[110:113]
	v_mfma_f32_16x16x32_bf16 v[94:97], v[114:117], v[212:215], v[94:97]
	v_mfma_f32_16x16x32_bf16 v[90:93], v[134:137], v[212:215], v[90:93]
	v_mfma_f32_16x16x32_bf16 v[78:81], v[114:117], v[220:223], v[78:81]
	v_mfma_f32_16x16x32_bf16 v[74:77], v[134:137], v[220:223], v[74:77]
	s_setprio 0
	s_setprio 1
	v_mfma_f32_16x16x32_bf16 v[130:133], v[138:141], v[166:169], v[130:133]
	v_mfma_f32_16x16x32_bf16 v[122:125], v[154:157], v[166:169], v[122:125]
	v_mfma_f32_16x16x32_bf16 v[106:109], v[138:141], v[200:203], v[106:109]
	v_mfma_f32_16x16x32_bf16 v[98:101], v[154:157], v[200:203], v[98:101]
	v_mfma_f32_16x16x32_bf16 v[86:89], v[138:141], v[208:211], v[86:89]
	v_mfma_f32_16x16x32_bf16 v[82:85], v[154:157], v[208:211], v[82:85]
	v_mfma_f32_16x16x32_bf16 v[70:73], v[138:141], v[216:219], v[70:73]
	v_mfma_f32_16x16x32_bf16 v[66:69], v[154:157], v[216:219], v[66:69]
	v_mfma_f32_16x16x32_bf16 v[130:133], v[146:149], v[176:179], v[130:133]
	v_mfma_f32_16x16x32_bf16 v[122:125], v[158:161], v[176:179], v[122:125]
	v_mfma_f32_16x16x32_bf16 v[106:109], v[146:149], v[204:207], v[106:109]
	v_mfma_f32_16x16x32_bf16 v[98:101], v[158:161], v[204:207], v[98:101]
	v_mfma_f32_16x16x32_bf16 v[86:89], v[146:149], v[212:215], v[86:89]
	v_mfma_f32_16x16x32_bf16 v[82:85], v[158:161], v[212:215], v[82:85]
	v_mfma_f32_16x16x32_bf16 v[70:73], v[146:149], v[220:223], v[70:73]
	v_mfma_f32_16x16x32_bf16 v[66:69], v[158:161], v[220:223], v[66:69]
	s_setprio 0
	s_barrier
	ds_read_b128 v[166:169], v173 offset:16384
	ds_read_b128 v[176:179], v173 offset:17408
	ds_read_b128 v[200:203], v173 offset:18432
	ds_read_b128 v[204:207], v173 offset:19456
	ds_read_b128 v[208:211], v173 offset:20480
	ds_read_b128 v[212:215], v173 offset:21504
	ds_read_b128 v[216:219], v173 offset:22528
	ds_read_b128 v[220:223], v173 offset:23552
	s_add_i32 s41, s44, s31
	v_lshl_add_u64 v[224:225], s[24:25], 0, v[162:163]
	s_mov_b32 m0, s41
	s_nop 0
	global_load_lds_dwordx4 v[224:225], off
	s_add_i32 m0, s41, 0x2000
	s_add_u32 s42, s24, 0x10000
	v_lshl_add_u64 v[226:227], s[24:25], 0, v[164:165]
	s_addc_u32 s43, s25, 0
	s_add_i32 s33, s33, s31
	global_load_lds_dwordx4 v[226:227], off
	v_lshl_add_u64 v[228:229], s[42:43], 0, v[162:163]
	s_mov_b32 m0, s33
	v_lshl_add_u64 v[230:231], s[26:27], 0, v[164:165]
	global_load_lds_dwordx4 v[228:229], off
	v_lshl_add_u64 v[228:229], s[42:43], 0, v[164:165]
	s_add_i32 m0, s33, 0x2000
	s_nop 0
	global_load_lds_dwordx4 v[228:229], off
	v_lshl_add_u64 v[228:229], s[26:27], 0, v[162:163]
	s_mov_b32 m0, s34
	s_nop 0
	global_load_lds_dwordx4 v[228:229], off
	s_mov_b32 m0, s35
	s_nop 0
	global_load_lds_dwordx4 v[230:231], off
	s_waitcnt vmcnt(8)
	s_waitcnt lgkmcnt(0)
	s_setprio 1
	s_barrier
	v_mfma_f32_16x16x32_bf16 v[62:65], v[102:105], v[166:169], v[62:65]
	v_mfma_f32_16x16x32_bf16 v[58:61], v[126:129], v[166:169], v[58:61]
	v_mfma_f32_16x16x32_bf16 v[46:49], v[102:105], v[200:203], v[46:49]
	v_mfma_f32_16x16x32_bf16 v[42:45], v[126:129], v[200:203], v[42:45]
	v_mfma_f32_16x16x32_bf16 v[30:33], v[102:105], v[208:211], v[30:33]
	v_mfma_f32_16x16x32_bf16 v[26:29], v[126:129], v[208:211], v[26:29]
	v_mfma_f32_16x16x32_bf16 v[14:17], v[102:105], v[216:219], v[14:17]
	v_mfma_f32_16x16x32_bf16 v[10:13], v[126:129], v[216:219], v[10:13]
	v_mfma_f32_16x16x32_bf16 v[62:65], v[114:117], v[176:179], v[62:65]
	v_mfma_f32_16x16x32_bf16 v[58:61], v[134:137], v[176:179], v[58:61]
	v_mfma_f32_16x16x32_bf16 v[46:49], v[114:117], v[204:207], v[46:49]
	v_mfma_f32_16x16x32_bf16 v[42:45], v[134:137], v[204:207], v[42:45]
	v_mfma_f32_16x16x32_bf16 v[30:33], v[114:117], v[212:215], v[30:33]
	v_mfma_f32_16x16x32_bf16 v[26:29], v[134:137], v[212:215], v[26:29]
	v_mfma_f32_16x16x32_bf16 v[14:17], v[114:117], v[220:223], v[14:17]
	v_mfma_f32_16x16x32_bf16 v[10:13], v[134:137], v[220:223], v[10:13]
	s_setprio 0
	s_setprio 1
	v_mfma_f32_16x16x32_bf16 v[54:57], v[138:141], v[166:169], v[54:57]
	v_mfma_f32_16x16x32_bf16 v[50:53], v[154:157], v[166:169], v[50:53]
	v_mfma_f32_16x16x32_bf16 v[38:41], v[138:141], v[200:203], v[38:41]
	v_mfma_f32_16x16x32_bf16 v[34:37], v[154:157], v[200:203], v[34:37]
	v_mfma_f32_16x16x32_bf16 v[22:25], v[138:141], v[208:211], v[22:25]
	v_mfma_f32_16x16x32_bf16 v[18:21], v[154:157], v[208:211], v[18:21]
	v_mfma_f32_16x16x32_bf16 v[6:9], v[138:141], v[216:219], v[6:9]
	v_mfma_f32_16x16x32_bf16 v[2:5], v[154:157], v[216:219], v[2:5]
	v_mfma_f32_16x16x32_bf16 v[54:57], v[146:149], v[176:179], v[54:57]
	v_mfma_f32_16x16x32_bf16 v[50:53], v[158:161], v[176:179], v[50:53]
	v_mfma_f32_16x16x32_bf16 v[38:41], v[146:149], v[204:207], v[38:41]
	v_mfma_f32_16x16x32_bf16 v[34:37], v[158:161], v[204:207], v[34:37]
	v_mfma_f32_16x16x32_bf16 v[22:25], v[146:149], v[212:215], v[22:25]
	v_mfma_f32_16x16x32_bf16 v[18:21], v[158:161], v[212:215], v[18:21]
	v_mfma_f32_16x16x32_bf16 v[6:9], v[146:149], v[220:223], v[6:9]
	v_mfma_f32_16x16x32_bf16 v[2:5], v[158:161], v[220:223], v[2:5]
	s_setprio 0
	s_barrier
	s_add_i32 s33, 0, 0x18000
	s_add_i32 s41, 0, 0x1c000
	v_add_u32_e32 v134, s33, v172
	v_add_u32_e32 v158, s41, v172
	ds_read_b128 v[102:105], v134
	ds_read_b128 v[114:117], v134 offset:1024
	ds_read_b128 v[126:129], v134 offset:2048
	ds_read_b128 v[134:137], v134 offset:3072
	ds_read_b128 v[138:141], v158
	ds_read_b128 v[146:149], v158 offset:1024
	ds_read_b128 v[154:157], v158 offset:2048
	ds_read_b128 v[158:161], v158 offset:3072
	ds_read_b128 v[166:169], v173 offset:32768
	ds_read_b128 v[176:179], v173 offset:33792
	ds_read_b128 v[200:203], v173 offset:34816
	ds_read_b128 v[204:207], v173 offset:35840
	ds_read_b128 v[208:211], v173 offset:36864
	ds_read_b128 v[212:215], v173 offset:37888
	ds_read_b128 v[216:219], v173 offset:38912
	ds_read_b128 v[220:223], v173 offset:39936
	s_add_u32 s26, s26, 0x10000
	s_addc_u32 s27, s27, 0
	s_mov_b32 m0, s36
	v_lshl_add_u64 v[232:233], s[26:27], 0, v[162:163]
	global_load_lds_dwordx4 v[232:233], off
	v_lshl_add_u64 v[232:233], s[26:27], 0, v[164:165]
	s_mov_b32 m0, s37
	s_nop 0
	global_load_lds_dwordx4 v[232:233], off
	s_waitcnt vmcnt(8)
	s_waitcnt lgkmcnt(0)
	s_setprio 1
	s_barrier
	v_mfma_f32_16x16x32_bf16 v[150:153], v[102:105], v[166:169], v[150:153]
	v_mfma_f32_16x16x32_bf16 v[142:145], v[126:129], v[166:169], v[142:145]
	v_mfma_f32_16x16x32_bf16 v[118:121], v[102:105], v[200:203], v[118:121]
	v_mfma_f32_16x16x32_bf16 v[110:113], v[126:129], v[200:203], v[110:113]
	v_mfma_f32_16x16x32_bf16 v[94:97], v[102:105], v[208:211], v[94:97]
	v_mfma_f32_16x16x32_bf16 v[90:93], v[126:129], v[208:211], v[90:93]
	v_mfma_f32_16x16x32_bf16 v[78:81], v[102:105], v[216:219], v[78:81]
	v_mfma_f32_16x16x32_bf16 v[74:77], v[126:129], v[216:219], v[74:77]
	v_mfma_f32_16x16x32_bf16 v[150:153], v[114:117], v[176:179], v[150:153]
	v_mfma_f32_16x16x32_bf16 v[142:145], v[134:137], v[176:179], v[142:145]
	v_mfma_f32_16x16x32_bf16 v[118:121], v[114:117], v[204:207], v[118:121]
	v_mfma_f32_16x16x32_bf16 v[110:113], v[134:137], v[204:207], v[110:113]
	v_mfma_f32_16x16x32_bf16 v[94:97], v[114:117], v[212:215], v[94:97]
	v_mfma_f32_16x16x32_bf16 v[90:93], v[134:137], v[212:215], v[90:93]
	v_mfma_f32_16x16x32_bf16 v[78:81], v[114:117], v[220:223], v[78:81]
	v_mfma_f32_16x16x32_bf16 v[74:77], v[134:137], v[220:223], v[74:77]
	s_setprio 0
	s_setprio 1
	v_mfma_f32_16x16x32_bf16 v[130:133], v[138:141], v[166:169], v[130:133]
	v_mfma_f32_16x16x32_bf16 v[122:125], v[154:157], v[166:169], v[122:125]
	v_mfma_f32_16x16x32_bf16 v[106:109], v[138:141], v[200:203], v[106:109]
	v_mfma_f32_16x16x32_bf16 v[98:101], v[154:157], v[200:203], v[98:101]
	v_mfma_f32_16x16x32_bf16 v[86:89], v[138:141], v[208:211], v[86:89]
	v_mfma_f32_16x16x32_bf16 v[82:85], v[154:157], v[208:211], v[82:85]
	v_mfma_f32_16x16x32_bf16 v[70:73], v[138:141], v[216:219], v[70:73]
	v_mfma_f32_16x16x32_bf16 v[66:69], v[154:157], v[216:219], v[66:69]
	v_mfma_f32_16x16x32_bf16 v[130:133], v[146:149], v[176:179], v[130:133]
	v_mfma_f32_16x16x32_bf16 v[122:125], v[158:161], v[176:179], v[122:125]
	v_mfma_f32_16x16x32_bf16 v[106:109], v[146:149], v[204:207], v[106:109]
	v_mfma_f32_16x16x32_bf16 v[98:101], v[158:161], v[204:207], v[98:101]
	v_mfma_f32_16x16x32_bf16 v[86:89], v[146:149], v[212:215], v[86:89]
	v_mfma_f32_16x16x32_bf16 v[82:85], v[158:161], v[212:215], v[82:85]
	v_mfma_f32_16x16x32_bf16 v[70:73], v[146:149], v[220:223], v[70:73]
	v_mfma_f32_16x16x32_bf16 v[66:69], v[158:161], v[220:223], v[66:69]
	s_setprio 0
	s_barrier
	ds_read_b128 v[166:169], v173 offset:49152
	ds_read_b128 v[176:179], v173 offset:50176
	ds_read_b128 v[200:203], v173 offset:51200
	ds_read_b128 v[204:207], v173 offset:52224
	ds_read_b128 v[208:211], v173 offset:53248
	ds_read_b128 v[212:215], v173 offset:54272
	ds_read_b128 v[216:219], v173 offset:55296
	ds_read_b128 v[220:223], v173 offset:56320
	s_add_i32 s26, s33, s31
	v_lshl_add_u64 v[224:225], v[224:225], 0, s[90:91]
	s_mov_b32 m0, s26
	s_nop 0
	global_load_lds_dwordx4 v[224:225], off
	s_add_i32 m0, s26, 0x2000
	s_add_u32 s24, s24, 0x10080
	v_lshl_add_u64 v[224:225], v[226:227], 0, s[90:91]
	s_addc_u32 s25, s25, 0
	s_add_i32 s26, s41, s31
	global_load_lds_dwordx4 v[224:225], off
	v_lshl_add_u64 v[224:225], s[24:25], 0, v[162:163]
	s_mov_b32 m0, s26
	s_nop 0
	global_load_lds_dwordx4 v[224:225], off
	v_lshl_add_u64 v[224:225], s[24:25], 0, v[164:165]
	s_add_i32 m0, s26, 0x2000
	s_nop 0
	global_load_lds_dwordx4 v[224:225], off
	v_lshl_add_u64 v[224:225], v[228:229], 0, s[90:91]
	s_mov_b32 m0, s38
	s_nop 0
	global_load_lds_dwordx4 v[224:225], off
	v_lshl_add_u64 v[224:225], v[230:231], 0, s[90:91]
	s_mov_b32 m0, s39
	s_nop 0
	global_load_lds_dwordx4 v[224:225], off
	s_waitcnt vmcnt(8)
	s_waitcnt lgkmcnt(0)
	s_setprio 1
	s_barrier
	v_mfma_f32_16x16x32_bf16 v[62:65], v[102:105], v[166:169], v[62:65]
	v_mfma_f32_16x16x32_bf16 v[58:61], v[126:129], v[166:169], v[58:61]
	v_mfma_f32_16x16x32_bf16 v[46:49], v[102:105], v[200:203], v[46:49]
	v_mfma_f32_16x16x32_bf16 v[42:45], v[126:129], v[200:203], v[42:45]
	v_mfma_f32_16x16x32_bf16 v[30:33], v[102:105], v[208:211], v[30:33]
	v_mfma_f32_16x16x32_bf16 v[26:29], v[126:129], v[208:211], v[26:29]
	v_mfma_f32_16x16x32_bf16 v[14:17], v[102:105], v[216:219], v[14:17]
	v_mfma_f32_16x16x32_bf16 v[10:13], v[126:129], v[216:219], v[10:13]
	v_mfma_f32_16x16x32_bf16 v[62:65], v[114:117], v[176:179], v[62:65]
	v_mfma_f32_16x16x32_bf16 v[58:61], v[134:137], v[176:179], v[58:61]
	v_mfma_f32_16x16x32_bf16 v[46:49], v[114:117], v[204:207], v[46:49]
	v_mfma_f32_16x16x32_bf16 v[42:45], v[134:137], v[204:207], v[42:45]
	v_mfma_f32_16x16x32_bf16 v[30:33], v[114:117], v[212:215], v[30:33]
	v_mfma_f32_16x16x32_bf16 v[26:29], v[134:137], v[212:215], v[26:29]
	v_mfma_f32_16x16x32_bf16 v[14:17], v[114:117], v[220:223], v[14:17]
	v_mfma_f32_16x16x32_bf16 v[10:13], v[134:137], v[220:223], v[10:13]
	s_setprio 0
	s_setprio 1
	v_mfma_f32_16x16x32_bf16 v[54:57], v[138:141], v[166:169], v[54:57]
	v_mfma_f32_16x16x32_bf16 v[50:53], v[154:157], v[166:169], v[50:53]
	v_mfma_f32_16x16x32_bf16 v[38:41], v[138:141], v[200:203], v[38:41]
	v_mfma_f32_16x16x32_bf16 v[34:37], v[154:157], v[200:203], v[34:37]
	v_mfma_f32_16x16x32_bf16 v[22:25], v[138:141], v[208:211], v[22:25]
	v_mfma_f32_16x16x32_bf16 v[18:21], v[154:157], v[208:211], v[18:21]
	v_mfma_f32_16x16x32_bf16 v[6:9], v[138:141], v[216:219], v[6:9]
	v_mfma_f32_16x16x32_bf16 v[2:5], v[154:157], v[216:219], v[2:5]
	v_mfma_f32_16x16x32_bf16 v[54:57], v[146:149], v[176:179], v[54:57]
	v_mfma_f32_16x16x32_bf16 v[50:53], v[158:161], v[176:179], v[50:53]
	v_mfma_f32_16x16x32_bf16 v[38:41], v[146:149], v[204:207], v[38:41]
	v_mfma_f32_16x16x32_bf16 v[34:37], v[158:161], v[204:207], v[34:37]
	v_mfma_f32_16x16x32_bf16 v[22:25], v[146:149], v[212:215], v[22:25]
	v_mfma_f32_16x16x32_bf16 v[18:21], v[158:161], v[212:215], v[18:21]
	v_mfma_f32_16x16x32_bf16 v[6:9], v[146:149], v[220:223], v[6:9]
	v_mfma_f32_16x16x32_bf16 v[2:5], v[158:161], v[220:223], v[2:5]
	s_setprio 0
	s_barrier
	s_and_b64 vcc, exec, s[22:23]
	s_mov_b64 s[24:25], -1
	s_mov_b64 s[22:23], 0
	s_movk_i32 s26, 0x100
	s_cbranch_vccnz .LBB0_843
	s_andn2_b64 vcc, exec, s[10:11]
	s_cbranch_vccnz .LBB0_846
	s_barrier

.LBB0_996:
	s_add_i32 s45, 0, 0x10000
	s_add_i32 s48, 0, 0x14000
	v_add_u32_e32 v142, s45, v171
	v_add_u32_e32 v168, s48, v171
	ds_read_b128 v[130:133], v142
	ds_read_b128 v[134:137], v142 offset:1024
	ds_read_b128 v[138:141], v142 offset:2048
	ds_read_b128 v[142:145], v142 offset:3072
	ds_read_b128 v[146:149], v168
	ds_read_b128 v[158:161], v168 offset:1024
	ds_read_b128 v[164:167], v168 offset:2048
	ds_read_b128 v[174:177], v168 offset:3072
	ds_read_b128 v[200:203], v172
	ds_read_b128 v[204:207], v172 offset:1024
	ds_read_b128 v[208:211], v172 offset:2048
	ds_read_b128 v[212:215], v172 offset:3072
	ds_read_b128 v[216:219], v172 offset:4096
	ds_read_b128 v[220:223], v172 offset:5120
	ds_read_b128 v[224:227], v172 offset:6144
	ds_read_b128 v[228:231], v172 offset:7168
	s_add_u32 s22, s20, 0xfffc0080
	s_addc_u32 s23, s21, -1
	s_cmp_eq_u32 s44, 12
	s_cselect_b32 s25, s9, s23
	s_cselect_b32 s24, s40, s22
	s_cselect_b32 s23, s11, s43
	s_cselect_b32 s22, s41, s42
	v_lshl_add_u64 v[168:169], s[20:21], 0, v[156:157]
	s_add_i32 m0, s33, 0xc000
	s_nop 0
	global_load_lds_dwordx4 v[168:169], off
	v_lshl_add_u64 v[168:169], s[20:21], 0, v[154:155]
	s_add_i32 m0, s33, 0xe000
	s_nop 0
	global_load_lds_dwordx4 v[168:169], off
	s_waitcnt vmcnt(8)
	s_waitcnt lgkmcnt(0)
	s_setprio 1
	s_barrier
	v_mfma_f32_16x16x32_bf16 v[126:129], v[130:133], v[200:203], v[126:129]
	v_mfma_f32_16x16x32_bf16 v[122:125], v[138:141], v[200:203], v[122:125]
	v_mfma_f32_16x16x32_bf16 v[110:113], v[130:133], v[208:211], v[110:113]
	v_mfma_f32_16x16x32_bf16 v[106:109], v[138:141], v[208:211], v[106:109]
	v_mfma_f32_16x16x32_bf16 v[98:101], v[130:133], v[216:219], v[98:101]
	v_mfma_f32_16x16x32_bf16 v[90:93], v[138:141], v[216:219], v[90:93]
	v_mfma_f32_16x16x32_bf16 v[86:89], v[130:133], v[224:227], v[86:89]
	v_mfma_f32_16x16x32_bf16 v[78:81], v[138:141], v[224:227], v[78:81]
	v_mfma_f32_16x16x32_bf16 v[126:129], v[134:137], v[204:207], v[126:129]
	v_mfma_f32_16x16x32_bf16 v[122:125], v[142:145], v[204:207], v[122:125]
	v_mfma_f32_16x16x32_bf16 v[110:113], v[134:137], v[212:215], v[110:113]
	v_mfma_f32_16x16x32_bf16 v[106:109], v[142:145], v[212:215], v[106:109]
	v_mfma_f32_16x16x32_bf16 v[98:101], v[134:137], v[220:223], v[98:101]
	v_mfma_f32_16x16x32_bf16 v[90:93], v[142:145], v[220:223], v[90:93]
	v_mfma_f32_16x16x32_bf16 v[86:89], v[134:137], v[228:231], v[86:89]
	v_mfma_f32_16x16x32_bf16 v[78:81], v[142:145], v[228:231], v[78:81]
	s_setprio 0
	s_setprio 1
	v_mfma_f32_16x16x32_bf16 v[118:121], v[146:149], v[200:203], v[118:121]
	v_mfma_f32_16x16x32_bf16 v[114:117], v[164:167], v[200:203], v[114:117]
	v_mfma_f32_16x16x32_bf16 v[102:105], v[146:149], v[208:211], v[102:105]
	v_mfma_f32_16x16x32_bf16 v[94:97], v[164:167], v[208:211], v[94:97]
	v_mfma_f32_16x16x32_bf16 v[82:85], v[146:149], v[216:219], v[82:85]
	v_mfma_f32_16x16x32_bf16 v[74:77], v[164:167], v[216:219], v[74:77]
	v_mfma_f32_16x16x32_bf16 v[70:73], v[146:149], v[224:227], v[70:73]
	v_mfma_f32_16x16x32_bf16 v[66:69], v[164:167], v[224:227], v[66:69]
	v_mfma_f32_16x16x32_bf16 v[118:121], v[158:161], v[204:207], v[118:121]
	v_mfma_f32_16x16x32_bf16 v[114:117], v[174:177], v[204:207], v[114:117]
	v_mfma_f32_16x16x32_bf16 v[102:105], v[158:161], v[212:215], v[102:105]
	v_mfma_f32_16x16x32_bf16 v[94:97], v[174:177], v[212:215], v[94:97]
	v_mfma_f32_16x16x32_bf16 v[82:85], v[158:161], v[220:223], v[82:85]
	v_mfma_f32_16x16x32_bf16 v[74:77], v[174:177], v[220:223], v[74:77]
	v_mfma_f32_16x16x32_bf16 v[70:73], v[158:161], v[228:231], v[70:73]
	v_mfma_f32_16x16x32_bf16 v[66:69], v[174:177], v[228:231], v[66:69]
	s_setprio 0
	s_barrier
	ds_read_b128 v[200:203], v172 offset:16384
	ds_read_b128 v[204:207], v172 offset:17408
	ds_read_b128 v[208:211], v172 offset:18432
	ds_read_b128 v[212:215], v172 offset:19456
	ds_read_b128 v[216:219], v172 offset:20480
	ds_read_b128 v[220:223], v172 offset:21504
	ds_read_b128 v[224:227], v172 offset:22528
	ds_read_b128 v[228:231], v172 offset:23552
	s_add_i32 s45, s45, s31
	v_lshl_add_u64 v[168:169], s[22:23], 0, v[162:163]
	s_mov_b32 m0, s45
	s_nop 0
	global_load_lds_dwordx4 v[168:169], off
	s_add_i32 m0, s45, 0x2000
	s_add_u32 s46, s22, 0x40000
	v_lshl_add_u64 v[178:179], s[22:23], 0, v[150:151]
	s_addc_u32 s47, s23, 0
	s_add_i32 s45, s48, s31
	global_load_lds_dwordx4 v[178:179], off
	v_lshl_add_u64 v[232:233], s[46:47], 0, v[162:163]
	s_mov_b32 m0, s45
	v_lshl_add_u64 v[234:235], s[24:25], 0, v[150:151]
	global_load_lds_dwordx4 v[232:233], off
	v_lshl_add_u64 v[232:233], s[46:47], 0, v[150:151]
	s_add_i32 m0, s45, 0x2000
	s_nop 0
	global_load_lds_dwordx4 v[232:233], off
	v_lshl_add_u64 v[232:233], s[24:25], 0, v[162:163]
	s_mov_b32 m0, s33
	s_nop 0
	global_load_lds_dwordx4 v[232:233], off
	s_mov_b32 m0, s34
	s_nop 0
	global_load_lds_dwordx4 v[234:235], off
	s_waitcnt vmcnt(8)
	s_waitcnt lgkmcnt(0)
	s_setprio 1
	s_barrier
	v_mfma_f32_16x16x32_bf16 v[62:65], v[130:133], v[200:203], v[62:65]
	v_mfma_f32_16x16x32_bf16 v[58:61], v[138:141], v[200:203], v[58:61]
	v_mfma_f32_16x16x32_bf16 v[50:53], v[130:133], v[208:211], v[50:53]
	v_mfma_f32_16x16x32_bf16 v[42:45], v[138:141], v[208:211], v[42:45]
	v_mfma_f32_16x16x32_bf16 v[34:37], v[130:133], v[216:219], v[34:37]
	v_mfma_f32_16x16x32_bf16 v[26:29], v[138:141], v[216:219], v[26:29]
	v_mfma_f32_16x16x32_bf16 v[18:21], v[130:133], v[224:227], v[18:21]
	v_mfma_f32_16x16x32_bf16 v[10:13], v[138:141], v[224:227], v[10:13]
	v_mfma_f32_16x16x32_bf16 v[62:65], v[134:137], v[204:207], v[62:65]
	v_mfma_f32_16x16x32_bf16 v[58:61], v[142:145], v[204:207], v[58:61]
	v_mfma_f32_16x16x32_bf16 v[50:53], v[134:137], v[212:215], v[50:53]
	v_mfma_f32_16x16x32_bf16 v[42:45], v[142:145], v[212:215], v[42:45]
	v_mfma_f32_16x16x32_bf16 v[34:37], v[134:137], v[220:223], v[34:37]
	v_mfma_f32_16x16x32_bf16 v[26:29], v[142:145], v[220:223], v[26:29]
	v_mfma_f32_16x16x32_bf16 v[18:21], v[134:137], v[228:231], v[18:21]
	v_mfma_f32_16x16x32_bf16 v[10:13], v[142:145], v[228:231], v[10:13]
	s_setprio 0
	s_setprio 1
	v_mfma_f32_16x16x32_bf16 v[54:57], v[146:149], v[200:203], v[54:57]
	v_mfma_f32_16x16x32_bf16 v[46:49], v[164:167], v[200:203], v[46:49]
	v_mfma_f32_16x16x32_bf16 v[38:41], v[146:149], v[208:211], v[38:41]
	v_mfma_f32_16x16x32_bf16 v[30:33], v[164:167], v[208:211], v[30:33]
	v_mfma_f32_16x16x32_bf16 v[22:25], v[146:149], v[216:219], v[22:25]
	v_mfma_f32_16x16x32_bf16 v[14:17], v[164:167], v[216:219], v[14:17]
	v_mfma_f32_16x16x32_bf16 v[6:9], v[146:149], v[224:227], v[6:9]
	v_mfma_f32_16x16x32_bf16 v[2:5], v[164:167], v[224:227], v[2:5]
	v_mfma_f32_16x16x32_bf16 v[54:57], v[158:161], v[204:207], v[54:57]
	v_mfma_f32_16x16x32_bf16 v[46:49], v[174:177], v[204:207], v[46:49]
	v_mfma_f32_16x16x32_bf16 v[38:41], v[158:161], v[212:215], v[38:41]
	v_mfma_f32_16x16x32_bf16 v[30:33], v[174:177], v[212:215], v[30:33]
	v_mfma_f32_16x16x32_bf16 v[22:25], v[158:161], v[220:223], v[22:25]
	v_mfma_f32_16x16x32_bf16 v[14:17], v[174:177], v[220:223], v[14:17]
	v_mfma_f32_16x16x32_bf16 v[6:9], v[158:161], v[228:231], v[6:9]
	v_mfma_f32_16x16x32_bf16 v[2:5], v[174:177], v[228:231], v[2:5]
	s_setprio 0
	s_barrier
	s_add_i32 s45, 0, 0x18000
	s_add_i32 s46, 0, 0x1c000
	v_add_u32_e32 v142, s45, v171
	v_add_u32_e32 v173, s46, v171
	ds_read_b128 v[130:133], v142
	ds_read_b128 v[134:137], v142 offset:1024
	ds_read_b128 v[138:141], v142 offset:2048
	ds_read_b128 v[142:145], v142 offset:3072
	ds_read_b128 v[146:149], v173
	ds_read_b128 v[158:161], v173 offset:1024
	ds_read_b128 v[164:167], v173 offset:2048
	ds_read_b128 v[174:177], v173 offset:3072
	ds_read_b128 v[200:203], v172 offset:32768
	ds_read_b128 v[204:207], v172 offset:33792
	ds_read_b128 v[208:211], v172 offset:34816
	ds_read_b128 v[212:215], v172 offset:35840
	ds_read_b128 v[216:219], v172 offset:36864
	ds_read_b128 v[220:223], v172 offset:37888
	ds_read_b128 v[224:227], v172 offset:38912
	ds_read_b128 v[228:231], v172 offset:39936
	s_add_u32 s24, s24, 0x40000
	s_addc_u32 s25, s25, 0
	s_mov_b32 m0, s35
	v_lshl_add_u64 v[236:237], s[24:25], 0, v[162:163]
	global_load_lds_dwordx4 v[236:237], off
	v_lshl_add_u64 v[236:237], s[24:25], 0, v[150:151]
	s_mov_b32 m0, s36
	s_nop 0
	global_load_lds_dwordx4 v[236:237], off
	s_waitcnt vmcnt(8)
	s_waitcnt lgkmcnt(0)
	s_setprio 1
	s_barrier
	v_mfma_f32_16x16x32_bf16 v[126:129], v[130:133], v[200:203], v[126:129]
	v_mfma_f32_16x16x32_bf16 v[122:125], v[138:141], v[200:203], v[122:125]
	v_mfma_f32_16x16x32_bf16 v[110:113], v[130:133], v[208:211], v[110:113]
	v_mfma_f32_16x16x32_bf16 v[106:109], v[138:141], v[208:211], v[106:109]
	v_mfma_f32_16x16x32_bf16 v[98:101], v[130:133], v[216:219], v[98:101]
	v_mfma_f32_16x16x32_bf16 v[90:93], v[138:141], v[216:219], v[90:93]
	v_mfma_f32_16x16x32_bf16 v[86:89], v[130:133], v[224:227], v[86:89]
	v_mfma_f32_16x16x32_bf16 v[78:81], v[138:141], v[224:227], v[78:81]
	v_mfma_f32_16x16x32_bf16 v[126:129], v[134:137], v[204:207], v[126:129]
	v_mfma_f32_16x16x32_bf16 v[122:125], v[142:145], v[204:207], v[122:125]
	v_mfma_f32_16x16x32_bf16 v[110:113], v[134:137], v[212:215], v[110:113]
	v_mfma_f32_16x16x32_bf16 v[106:109], v[142:145], v[212:215], v[106:109]
	v_mfma_f32_16x16x32_bf16 v[98:101], v[134:137], v[220:223], v[98:101]
	v_mfma_f32_16x16x32_bf16 v[90:93], v[142:145], v[220:223], v[90:93]
	v_mfma_f32_16x16x32_bf16 v[86:89], v[134:137], v[228:231], v[86:89]
	v_mfma_f32_16x16x32_bf16 v[78:81], v[142:145], v[228:231], v[78:81]
	s_setprio 0
	s_setprio 1
	v_mfma_f32_16x16x32_bf16 v[118:121], v[146:149], v[200:203], v[118:121]
	v_mfma_f32_16x16x32_bf16 v[114:117], v[164:167], v[200:203], v[114:117]
	v_mfma_f32_16x16x32_bf16 v[102:105], v[146:149], v[208:211], v[102:105]
	v_mfma_f32_16x16x32_bf16 v[94:97], v[164:167], v[208:211], v[94:97]
	v_mfma_f32_16x16x32_bf16 v[82:85], v[146:149], v[216:219], v[82:85]
	v_mfma_f32_16x16x32_bf16 v[74:77], v[164:167], v[216:219], v[74:77]
	v_mfma_f32_16x16x32_bf16 v[70:73], v[146:149], v[224:227], v[70:73]
	v_mfma_f32_16x16x32_bf16 v[66:69], v[164:167], v[224:227], v[66:69]
	v_mfma_f32_16x16x32_bf16 v[118:121], v[158:161], v[204:207], v[118:121]
	v_mfma_f32_16x16x32_bf16 v[114:117], v[174:177], v[204:207], v[114:117]
	v_mfma_f32_16x16x32_bf16 v[102:105], v[158:161], v[212:215], v[102:105]
	v_mfma_f32_16x16x32_bf16 v[94:97], v[174:177], v[212:215], v[94:97]
	v_mfma_f32_16x16x32_bf16 v[82:85], v[158:161], v[220:223], v[82:85]
	v_mfma_f32_16x16x32_bf16 v[74:77], v[174:177], v[220:223], v[74:77]
	v_mfma_f32_16x16x32_bf16 v[70:73], v[158:161], v[228:231], v[70:73]
	v_mfma_f32_16x16x32_bf16 v[66:69], v[174:177], v[228:231], v[66:69]
	s_setprio 0
	s_barrier
	ds_read_b128 v[200:203], v172 offset:49152
	ds_read_b128 v[204:207], v172 offset:50176
	ds_read_b128 v[208:211], v172 offset:51200
	ds_read_b128 v[212:215], v172 offset:52224
	ds_read_b128 v[216:219], v172 offset:53248
	ds_read_b128 v[220:223], v172 offset:54272
	ds_read_b128 v[224:227], v172 offset:55296
	ds_read_b128 v[228:231], v172 offset:56320
	s_add_i32 s24, s45, s31
	v_lshl_add_u64 v[168:169], v[168:169], 0, s[90:91]
	s_mov_b32 m0, s24
	s_nop 0
	global_load_lds_dwordx4 v[168:169], off
	s_add_i32 m0, s24, 0x2000
	s_add_u32 s22, s22, 0x40080
	v_lshl_add_u64 v[168:169], v[178:179], 0, s[90:91]
	s_addc_u32 s23, s23, 0
	s_add_i32 s24, s46, s31
	global_load_lds_dwordx4 v[168:169], off
	v_lshl_add_u64 v[168:169], s[22:23], 0, v[162:163]
	s_mov_b32 m0, s24
	s_nop 0
	global_load_lds_dwordx4 v[168:169], off
	v_lshl_add_u64 v[168:169], s[22:23], 0, v[150:151]
	s_add_i32 m0, s24, 0x2000
	s_nop 0
	global_load_lds_dwordx4 v[168:169], off
	v_lshl_add_u64 v[168:169], v[232:233], 0, s[90:91]
	s_mov_b32 m0, s37
	s_nop 0
	global_load_lds_dwordx4 v[168:169], off
	v_lshl_add_u64 v[168:169], v[234:235], 0, s[90:91]
	s_mov_b32 m0, s38
	s_nop 0
	global_load_lds_dwordx4 v[168:169], off
	s_waitcnt vmcnt(8)
	s_waitcnt lgkmcnt(0)
	s_setprio 1
	s_barrier
	v_mfma_f32_16x16x32_bf16 v[62:65], v[130:133], v[200:203], v[62:65]
	v_mfma_f32_16x16x32_bf16 v[58:61], v[138:141], v[200:203], v[58:61]
	v_mfma_f32_16x16x32_bf16 v[50:53], v[130:133], v[208:211], v[50:53]
	v_mfma_f32_16x16x32_bf16 v[42:45], v[138:141], v[208:211], v[42:45]
	v_mfma_f32_16x16x32_bf16 v[34:37], v[130:133], v[216:219], v[34:37]
	v_mfma_f32_16x16x32_bf16 v[26:29], v[138:141], v[216:219], v[26:29]
	v_mfma_f32_16x16x32_bf16 v[18:21], v[130:133], v[224:227], v[18:21]
	v_mfma_f32_16x16x32_bf16 v[10:13], v[138:141], v[224:227], v[10:13]
	v_mfma_f32_16x16x32_bf16 v[62:65], v[134:137], v[204:207], v[62:65]
	v_mfma_f32_16x16x32_bf16 v[58:61], v[142:145], v[204:207], v[58:61]
	v_mfma_f32_16x16x32_bf16 v[50:53], v[134:137], v[212:215], v[50:53]
	v_mfma_f32_16x16x32_bf16 v[42:45], v[142:145], v[212:215], v[42:45]
	v_mfma_f32_16x16x32_bf16 v[34:37], v[134:137], v[220:223], v[34:37]
	v_mfma_f32_16x16x32_bf16 v[26:29], v[142:145], v[220:223], v[26:29]
	v_mfma_f32_16x16x32_bf16 v[18:21], v[134:137], v[228:231], v[18:21]
	v_mfma_f32_16x16x32_bf16 v[10:13], v[142:145], v[228:231], v[10:13]
	s_setprio 0
	s_setprio 1
	v_mfma_f32_16x16x32_bf16 v[54:57], v[146:149], v[200:203], v[54:57]
	v_mfma_f32_16x16x32_bf16 v[46:49], v[164:167], v[200:203], v[46:49]
	v_mfma_f32_16x16x32_bf16 v[38:41], v[146:149], v[208:211], v[38:41]
	v_mfma_f32_16x16x32_bf16 v[30:33], v[164:167], v[208:211], v[30:33]
	v_mfma_f32_16x16x32_bf16 v[22:25], v[146:149], v[216:219], v[22:25]
	v_mfma_f32_16x16x32_bf16 v[14:17], v[164:167], v[216:219], v[14:17]
	v_mfma_f32_16x16x32_bf16 v[6:9], v[146:149], v[224:227], v[6:9]
	v_mfma_f32_16x16x32_bf16 v[2:5], v[164:167], v[224:227], v[2:5]
	v_mfma_f32_16x16x32_bf16 v[54:57], v[158:161], v[204:207], v[54:57]
	v_mfma_f32_16x16x32_bf16 v[46:49], v[174:177], v[204:207], v[46:49]
	v_mfma_f32_16x16x32_bf16 v[38:41], v[158:161], v[212:215], v[38:41]
	v_mfma_f32_16x16x32_bf16 v[30:33], v[174:177], v[212:215], v[30:33]
	v_mfma_f32_16x16x32_bf16 v[22:25], v[158:161], v[220:223], v[22:25]
	v_mfma_f32_16x16x32_bf16 v[14:17], v[174:177], v[220:223], v[14:17]
	v_mfma_f32_16x16x32_bf16 v[6:9], v[158:161], v[228:231], v[6:9]
	v_mfma_f32_16x16x32_bf16 v[2:5], v[174:177], v[228:231], v[2:5]
	s_setprio 0
	s_barrier
	s_add_i32 s44, s44, 2
	s_add_u32 s42, s42, 0x100
	s_addc_u32 s43, s43, 0
	s_add_u32 s20, s20, 0x100
	s_addc_u32 s21, s21, 0
	s_cmp_lt_u32 s44, 14
	s_cbranch_scc1 .LBB0_996
	v_readlane_b32 s40, v254, 24
	s_andn2_b64 vcc, exec, s[6:7]
	v_readlane_b32 s42, v254, 26
	v_readlane_b32 s43, v254, 27
	v_readlane_b32 s44, v254, 28
	v_readlane_b32 s45, v254, 29
	v_readlane_b32 s46, v254, 30
	v_readlane_b32 s47, v254, 31
	v_readlane_b32 s50, v254, 34
	v_readlane_b32 s51, v254, 35
	v_readlane_b32 s41, v254, 25
	v_readlane_b32 s48, v254, 32
	v_readlane_b32 s49, v254, 33
	v_readlane_b32 s52, v254, 36
	v_readlane_b32 s53, v254, 37
	v_readlane_b32 s54, v254, 38
	v_readlane_b32 s55, v254, 39
	s_cbranch_vccnz .LBB0_999
	s_barrier

.LBB0_1374:
	ds_read_b128 v[2:5], v202
	ds_read_b128 v[6:9], v203
	ds_read_b128 v[18:21], v204
	ds_read_b128 v[22:25], v205
	ds_read_b128 v[26:29], v206
	ds_read_b128 v[30:33], v207
	ds_read_b128 v[172:175], v208
	ds_read_b128 v[176:179], v209
	ds_read_b128 v[10:13], v218
	ds_read_b128 v[14:17], v218 offset:1024
	ds_read_b128 v[220:223], v218 offset:2048
	ds_read_b128 v[224:227], v218 offset:3072
	ds_read_b128 v[228:231], v218 offset:4096
	ds_read_b128 v[232:235], v218 offset:5120
	ds_read_b128 v[236:239], v218 offset:6144
	ds_read_b128 v[240:243], v218 offset:7168
	s_add_u32 s22, s20, 0xfffc0080
	s_addc_u32 s23, s21, -1
	s_cmp_eq_u32 s51, 12
	s_cselect_b32 s25, s11, s23
	s_cselect_b32 s24, s13, s22
	s_cselect_b32 s23, s15, s50
	s_cselect_b32 s22, s14, s49
	s_mov_b32 m0, s47
	v_lshl_add_u64 v[244:245], s[20:21], 0, v[170:171]
	global_load_lds_dwordx4 v[244:245], off
	v_lshl_add_u64 v[244:245], s[20:21], 0, v[168:169]
	s_mov_b32 m0, s48
	s_nop 0
	global_load_lds_dwordx4 v[244:245], off
	s_waitcnt vmcnt(8)
	s_waitcnt lgkmcnt(0)
	s_setprio 1
	s_barrier
	v_mfma_f32_16x16x128_f8f6f4 v[158:161], v[2:9], v[10:17], v[158:161]
	v_mfma_f32_16x16x128_f8f6f4 v[154:157], v[18:25], v[10:17], v[154:157]
	v_mfma_f32_16x16x128_f8f6f4 v[150:153], v[2:9], v[220:227], v[150:153]
	v_mfma_f32_16x16x128_f8f6f4 v[146:149], v[18:25], v[220:227], v[146:149]
	v_mfma_f32_16x16x128_f8f6f4 v[126:129], v[2:9], v[228:235], v[126:129]
	v_mfma_f32_16x16x128_f8f6f4 v[122:125], v[18:25], v[228:235], v[122:125]
	v_mfma_f32_16x16x128_f8f6f4 v[118:121], v[2:9], v[236:243], v[118:121]
	v_mfma_f32_16x16x128_f8f6f4 v[114:117], v[18:25], v[236:243], v[114:117]
	s_setprio 0
	s_setprio 1
	v_mfma_f32_16x16x128_f8f6f4 v[142:145], v[26:33], v[10:17], v[142:145]
	v_mfma_f32_16x16x128_f8f6f4 v[138:141], v[172:179], v[10:17], v[138:141]
	v_mfma_f32_16x16x128_f8f6f4 v[134:137], v[26:33], v[220:227], v[134:137]
	v_mfma_f32_16x16x128_f8f6f4 v[130:133], v[172:179], v[220:227], v[130:133]
	v_mfma_f32_16x16x128_f8f6f4 v[110:113], v[26:33], v[228:235], v[110:113]
	v_mfma_f32_16x16x128_f8f6f4 v[106:109], v[172:179], v[228:235], v[106:109]
	v_mfma_f32_16x16x128_f8f6f4 v[98:101], v[26:33], v[236:243], v[98:101]
	v_mfma_f32_16x16x128_f8f6f4 v[90:93], v[172:179], v[236:243], v[90:93]
	s_setprio 0
	s_barrier
	ds_read_b128 v[220:223], v218 offset:16384
	ds_read_b128 v[224:227], v218 offset:17408
	ds_read_b128 v[228:231], v218 offset:18432
	ds_read_b128 v[232:235], v218 offset:19456
	ds_read_b128 v[236:239], v218 offset:20480
	ds_read_b128 v[240:243], v218 offset:21504
	ds_read_b128 v[244:247], v218 offset:22528
	ds_read_b128 v[248:251], v218 offset:23552
	s_mov_b32 m0, s33
	v_lshl_add_u64 v[10:11], s[22:23], 0, v[162:163]
	s_add_u32 s52, s22, 0x40000
	global_load_lds_dwordx4 v[10:11], off
	v_lshl_add_u64 v[12:13], s[22:23], 0, v[164:165]
	s_mov_b32 m0, s34
	s_addc_u32 s53, s23, 0
	global_load_lds_dwordx4 v[12:13], off
	v_lshl_add_u64 v[14:15], s[52:53], 0, v[162:163]
	s_mov_b32 m0, s35
	v_lshl_add_u64 v[16:17], s[24:25], 0, v[164:165]
	global_load_lds_dwordx4 v[14:15], off
	v_lshl_add_u64 v[14:15], s[52:53], 0, v[164:165]
	s_mov_b32 m0, s36
	s_nop 0
	global_load_lds_dwordx4 v[14:15], off
	v_lshl_add_u64 v[14:15], s[24:25], 0, v[162:163]
	s_mov_b32 m0, s31
	s_nop 0
	global_load_lds_dwordx4 v[14:15], off
	s_mov_b32 m0, s37
	s_nop 0
	global_load_lds_dwordx4 v[16:17], off
	s_waitcnt vmcnt(8)
	s_waitcnt lgkmcnt(0)
	s_setprio 1
	s_barrier
	v_mfma_f32_16x16x128_f8f6f4 v[102:105], v[2:9], v[220:227], v[102:105]
	v_mfma_f32_16x16x128_f8f6f4 v[94:97], v[18:25], v[220:227], v[94:97]
	v_mfma_f32_16x16x128_f8f6f4 v[86:89], v[2:9], v[228:235], v[86:89]
	v_mfma_f32_16x16x128_f8f6f4 v[82:85], v[18:25], v[228:235], v[82:85]
	v_mfma_f32_16x16x128_f8f6f4 v[62:65], v[2:9], v[236:243], v[62:65]
	v_mfma_f32_16x16x128_f8f6f4 v[58:61], v[18:25], v[236:243], v[58:61]
	v_mfma_f32_16x16x128_f8f6f4 v[54:57], v[2:9], v[244:251], v[54:57]
	v_mfma_f32_16x16x128_f8f6f4 v[50:53], v[18:25], v[244:251], v[50:53]
	s_setprio 0
	s_setprio 1
	v_mfma_f32_16x16x128_f8f6f4 v[78:81], v[26:33], v[220:227], v[78:81]
	v_mfma_f32_16x16x128_f8f6f4 v[74:77], v[172:179], v[220:227], v[74:77]
	v_mfma_f32_16x16x128_f8f6f4 v[70:73], v[26:33], v[228:235], v[70:73]
	v_mfma_f32_16x16x128_f8f6f4 v[66:69], v[172:179], v[228:235], v[66:69]
	v_mfma_f32_16x16x128_f8f6f4 v[46:49], v[26:33], v[236:243], v[46:49]
	v_mfma_f32_16x16x128_f8f6f4 v[42:45], v[172:179], v[236:243], v[42:45]
	v_mfma_f32_16x16x128_f8f6f4 v[38:41], v[26:33], v[244:251], v[38:41]
	v_mfma_f32_16x16x128_f8f6f4 v[34:37], v[172:179], v[244:251], v[34:37]
	s_setprio 0
	s_barrier
	ds_read_b128 v[18:21], v210
	ds_read_b128 v[22:25], v211
	ds_read_b128 v[26:29], v212
	ds_read_b128 v[30:33], v213
	ds_read_b128 v[2:5], v214
	ds_read_b128 v[6:9], v215
	ds_read_b128 v[172:175], v216
	ds_read_b128 v[176:179], v217
	ds_read_b128 v[220:223], v218 offset:32768
	ds_read_b128 v[224:227], v218 offset:33792
	ds_read_b128 v[228:231], v218 offset:34816
	ds_read_b128 v[232:235], v218 offset:35840
	ds_read_b128 v[236:239], v218 offset:36864
	ds_read_b128 v[240:243], v218 offset:37888
	ds_read_b128 v[244:247], v218 offset:38912
	ds_read_b128 v[248:251], v218 offset:39936
	s_add_u32 s24, s24, 0x40000
	s_addc_u32 s25, s25, 0
	s_mov_b32 m0, s38
	v_lshl_add_u64 v[252:253], s[24:25], 0, v[162:163]
	global_load_lds_dwordx4 v[252:253], off
	v_lshl_add_u64 v[252:253], s[24:25], 0, v[164:165]
	s_mov_b32 m0, s39
	s_nop 0
	global_load_lds_dwordx4 v[252:253], off
	s_waitcnt vmcnt(8)
	s_waitcnt lgkmcnt(0)
	s_setprio 1
	s_barrier
	v_mfma_f32_16x16x128_f8f6f4 v[158:161], v[18:25], v[220:227], v[158:161]
	v_mfma_f32_16x16x128_f8f6f4 v[154:157], v[26:33], v[220:227], v[154:157]
	v_mfma_f32_16x16x128_f8f6f4 v[150:153], v[18:25], v[228:235], v[150:153]
	v_mfma_f32_16x16x128_f8f6f4 v[146:149], v[26:33], v[228:235], v[146:149]
	v_mfma_f32_16x16x128_f8f6f4 v[126:129], v[18:25], v[236:243], v[126:129]
	v_mfma_f32_16x16x128_f8f6f4 v[122:125], v[26:33], v[236:243], v[122:125]
	v_mfma_f32_16x16x128_f8f6f4 v[118:121], v[18:25], v[244:251], v[118:121]
	v_mfma_f32_16x16x128_f8f6f4 v[114:117], v[26:33], v[244:251], v[114:117]
	s_setprio 0
	s_setprio 1
	v_mfma_f32_16x16x128_f8f6f4 v[142:145], v[2:9], v[220:227], v[142:145]
	v_mfma_f32_16x16x128_f8f6f4 v[138:141], v[172:179], v[220:227], v[138:141]
	v_mfma_f32_16x16x128_f8f6f4 v[134:137], v[2:9], v[228:235], v[134:137]
	v_mfma_f32_16x16x128_f8f6f4 v[130:133], v[172:179], v[228:235], v[130:133]
	v_mfma_f32_16x16x128_f8f6f4 v[110:113], v[2:9], v[236:243], v[110:113]
	v_mfma_f32_16x16x128_f8f6f4 v[106:109], v[172:179], v[236:243], v[106:109]
	v_mfma_f32_16x16x128_f8f6f4 v[98:101], v[2:9], v[244:251], v[98:101]
	v_mfma_f32_16x16x128_f8f6f4 v[90:93], v[172:179], v[244:251], v[90:93]
	s_setprio 0
	s_barrier
	ds_read_b128 v[220:223], v218 offset:49152
	ds_read_b128 v[224:227], v218 offset:50176
	ds_read_b128 v[228:231], v218 offset:51200
	ds_read_b128 v[232:235], v218 offset:52224
	ds_read_b128 v[236:239], v218 offset:53248
	ds_read_b128 v[240:243], v218 offset:54272
	ds_read_b128 v[244:247], v218 offset:55296
	ds_read_b128 v[248:251], v218 offset:56320
	s_mov_b32 m0, s40
	v_lshl_add_u64 v[10:11], v[10:11], 0, s[90:91]
	s_add_u32 s22, s22, 0x40080
	global_load_lds_dwordx4 v[10:11], off
	v_lshl_add_u64 v[10:11], v[12:13], 0, s[90:91]
	s_mov_b32 m0, s41
	s_addc_u32 s23, s23, 0
	global_load_lds_dwordx4 v[10:11], off
	v_lshl_add_u64 v[10:11], s[22:23], 0, v[162:163]
	s_mov_b32 m0, s44
	s_nop 0
	global_load_lds_dwordx4 v[10:11], off
	v_lshl_add_u64 v[10:11], s[22:23], 0, v[164:165]
	s_mov_b32 m0, s45
	s_nop 0
	global_load_lds_dwordx4 v[10:11], off
	v_lshl_add_u64 v[10:11], v[14:15], 0, s[90:91]
	s_mov_b32 m0, s42
	s_nop 0
	global_load_lds_dwordx4 v[10:11], off
	v_lshl_add_u64 v[10:11], v[16:17], 0, s[90:91]
	s_mov_b32 m0, s43
	s_nop 0
	global_load_lds_dwordx4 v[10:11], off
	s_waitcnt vmcnt(8)
	s_waitcnt lgkmcnt(0)
	s_setprio 1
	s_barrier
	v_mfma_f32_16x16x128_f8f6f4 v[102:105], v[18:25], v[220:227], v[102:105]
	v_mfma_f32_16x16x128_f8f6f4 v[94:97], v[26:33], v[220:227], v[94:97]
	v_mfma_f32_16x16x128_f8f6f4 v[86:89], v[18:25], v[228:235], v[86:89]
	v_mfma_f32_16x16x128_f8f6f4 v[82:85], v[26:33], v[228:235], v[82:85]
	v_mfma_f32_16x16x128_f8f6f4 v[62:65], v[18:25], v[236:243], v[62:65]
	v_mfma_f32_16x16x128_f8f6f4 v[58:61], v[26:33], v[236:243], v[58:61]
	v_mfma_f32_16x16x128_f8f6f4 v[54:57], v[18:25], v[244:251], v[54:57]
	v_mfma_f32_16x16x128_f8f6f4 v[50:53], v[26:33], v[244:251], v[50:53]
	s_setprio 0
	s_setprio 1
	v_mfma_f32_16x16x128_f8f6f4 v[78:81], v[2:9], v[220:227], v[78:81]
	v_mfma_f32_16x16x128_f8f6f4 v[74:77], v[172:179], v[220:227], v[74:77]
	v_mfma_f32_16x16x128_f8f6f4 v[70:73], v[2:9], v[228:235], v[70:73]
	v_mfma_f32_16x16x128_f8f6f4 v[66:69], v[172:179], v[228:235], v[66:69]
	v_mfma_f32_16x16x128_f8f6f4 v[46:49], v[2:9], v[236:243], v[46:49]
	v_mfma_f32_16x16x128_f8f6f4 v[42:45], v[172:179], v[236:243], v[42:45]
	v_mfma_f32_16x16x128_f8f6f4 v[38:41], v[2:9], v[244:251], v[38:41]
	v_mfma_f32_16x16x128_f8f6f4 v[34:37], v[172:179], v[244:251], v[34:37]
	s_setprio 0
	s_barrier
	s_add_i32 s51, s51, 2
	s_add_u32 s49, s49, 0x100
	s_addc_u32 s50, s50, 0
	s_add_u32 s20, s20, 0x100
	s_addc_u32 s21, s21, 0
	s_cmp_lt_u32 s51, 14
	s_cbranch_scc1 .LBB0_1374
	s_andn2_b64 vcc, exec, s[8:9]
	s_cbranch_vccnz .LBB0_1377
	s_barrier
